# GEMM compute blocks reduced to 32 bare MFMAs (priority toggles and satisfied waits removed); operand-sharing MFMA order in 4 loops; forget-weight gather in one round trip
# baseline (speedup 1.0000x reference)
.LBB0_114:
	ds_read_b128 v[130:133], v220
	ds_read_b128 v[134:137], v220 offset:1024
	ds_read_b128 v[138:141], v220 offset:2048
	ds_read_b128 v[142:145], v220 offset:3072
	ds_read_b128 v[146:149], v221
	ds_read_b128 v[150:153], v221 offset:1024
	ds_read_b128 v[154:157], v221 offset:2048
	ds_read_b128 v[158:161], v221 offset:3072
	s_add_i32 s46, s64, 0xfff80080
	s_cmp_eq_u32 s84, 28
	s_cselect_b32 s87, s62, s46
	s_cselect_b32 s86, s63, s65
	s_or_b32 s85, s87, 0x80
	s_mov_b32 m0, s93
	ds_read_b128 v[162:165], v222
	ds_read_b128 v[166:169], v222 offset:1024
	ds_read_b128 v[170:173], v222 offset:2048
	ds_read_b128 v[174:177], v222 offset:3072
	ds_read_b128 v[178:181], v222 offset:4096
	ds_read_b128 v[182:185], v222 offset:5120
	ds_read_b128 v[186:189], v222 offset:6144
	ds_read_b128 v[212:215], v222 offset:7168
	buffer_load_dwordx4 v1, s[40:43], s64 offen lds
	s_mov_b32 m0, s94
	s_nop 0
	buffer_load_dwordx4 v216, s[40:43], s64 offen lds
	s_waitcnt vmcnt(8)
	s_waitcnt lgkmcnt(0)
	s_barrier
	v_mfma_f32_16x16x32_bf16 v[126:129], v[130:133], v[162:165], v[126:129]
	v_mfma_f32_16x16x32_bf16 v[122:125], v[138:141], v[162:165], v[122:125]
	v_mfma_f32_16x16x32_bf16 v[106:109], v[138:141], v[170:173], v[106:109]
	v_mfma_f32_16x16x32_bf16 v[114:117], v[130:133], v[170:173], v[114:117]
	v_mfma_f32_16x16x32_bf16 v[102:105], v[130:133], v[178:181], v[102:105]
	v_mfma_f32_16x16x32_bf16 v[94:97], v[138:141], v[178:181], v[94:97]
	v_mfma_f32_16x16x32_bf16 v[78:81], v[138:141], v[186:189], v[78:81]
	v_mfma_f32_16x16x32_bf16 v[86:89], v[130:133], v[186:189], v[86:89]
	v_mfma_f32_16x16x32_bf16 v[126:129], v[134:137], v[166:169], v[126:129]
	v_mfma_f32_16x16x32_bf16 v[122:125], v[142:145], v[166:169], v[122:125]
	v_mfma_f32_16x16x32_bf16 v[106:109], v[142:145], v[174:177], v[106:109]
	v_mfma_f32_16x16x32_bf16 v[114:117], v[134:137], v[174:177], v[114:117]
	v_mfma_f32_16x16x32_bf16 v[102:105], v[134:137], v[182:185], v[102:105]
	v_mfma_f32_16x16x32_bf16 v[94:97], v[142:145], v[182:185], v[94:97]
	v_mfma_f32_16x16x32_bf16 v[78:81], v[142:145], v[212:215], v[78:81]
	v_mfma_f32_16x16x32_bf16 v[86:89], v[134:137], v[212:215], v[86:89]
	v_mfma_f32_16x16x32_bf16 v[118:121], v[146:149], v[162:165], v[118:121]
	v_mfma_f32_16x16x32_bf16 v[110:113], v[154:157], v[162:165], v[110:113]
	v_mfma_f32_16x16x32_bf16 v[90:93], v[154:157], v[170:173], v[90:93]
	v_mfma_f32_16x16x32_bf16 v[98:101], v[146:149], v[170:173], v[98:101]
	v_mfma_f32_16x16x32_bf16 v[82:85], v[146:149], v[178:181], v[82:85]
	v_mfma_f32_16x16x32_bf16 v[74:77], v[154:157], v[178:181], v[74:77]
	v_mfma_f32_16x16x32_bf16 v[66:69], v[154:157], v[186:189], v[66:69]
	v_mfma_f32_16x16x32_bf16 v[70:73], v[146:149], v[186:189], v[70:73]
	v_mfma_f32_16x16x32_bf16 v[118:121], v[150:153], v[166:169], v[118:121]
	v_mfma_f32_16x16x32_bf16 v[110:113], v[158:161], v[166:169], v[110:113]
	v_mfma_f32_16x16x32_bf16 v[90:93], v[158:161], v[174:177], v[90:93]
	v_mfma_f32_16x16x32_bf16 v[98:101], v[150:153], v[174:177], v[98:101]
	v_mfma_f32_16x16x32_bf16 v[82:85], v[150:153], v[182:185], v[82:85]
	v_mfma_f32_16x16x32_bf16 v[74:77], v[158:161], v[182:185], v[74:77]
	v_mfma_f32_16x16x32_bf16 v[66:69], v[158:161], v[212:215], v[66:69]
	v_mfma_f32_16x16x32_bf16 v[70:73], v[150:153], v[212:215], v[70:73]
	s_barrier
	s_mov_b32 m0, s69
	s_mov_b32 s46, s42
	s_mov_b32 s47, s43
	ds_read_b128 v[162:165], v222 offset:16384
	ds_read_b128 v[166:169], v222 offset:17408
	ds_read_b128 v[170:173], v222 offset:18432
	ds_read_b128 v[174:177], v222 offset:19456
	ds_read_b128 v[178:181], v222 offset:20480
	ds_read_b128 v[182:185], v222 offset:21504
	ds_read_b128 v[186:189], v222 offset:22528
	ds_read_b128 v[212:215], v222 offset:23552
	buffer_load_dwordx4 v191, s[44:47], s86 offen lds
	s_mov_b32 m0, s70
	s_add_i32 s88, s86, 0x80000
	buffer_load_dwordx4 v217, s[44:47], s86 offen lds
	s_mov_b32 m0, s71
	s_nop 0
	buffer_load_dwordx4 v191, s[44:47], s88 offen lds
	s_mov_b32 m0, s72
	s_nop 0
	buffer_load_dwordx4 v217, s[44:47], s88 offen lds
	s_mov_b32 m0, s68
	s_nop 0
	buffer_load_dwordx4 v1, s[40:43], s87 offen lds
	s_mov_b32 m0, s73
	s_nop 0
	buffer_load_dwordx4 v216, s[40:43], s87 offen lds
	s_waitcnt vmcnt(8)
	s_waitcnt lgkmcnt(0)
	s_barrier
	v_mfma_f32_16x16x32_bf16 v[62:65], v[130:133], v[162:165], v[62:65]
	v_mfma_f32_16x16x32_bf16 v[58:61], v[138:141], v[162:165], v[58:61]
	v_mfma_f32_16x16x32_bf16 v[46:49], v[138:141], v[170:173], v[46:49]
	v_mfma_f32_16x16x32_bf16 v[54:57], v[130:133], v[170:173], v[54:57]
	v_mfma_f32_16x16x32_bf16 v[38:41], v[130:133], v[178:181], v[38:41]
	v_mfma_f32_16x16x32_bf16 v[30:33], v[138:141], v[178:181], v[30:33]
	v_mfma_f32_16x16x32_bf16 v[14:17], v[138:141], v[186:189], v[14:17]
	v_mfma_f32_16x16x32_bf16 v[22:25], v[130:133], v[186:189], v[22:25]
	v_mfma_f32_16x16x32_bf16 v[62:65], v[134:137], v[166:169], v[62:65]
	v_mfma_f32_16x16x32_bf16 v[58:61], v[142:145], v[166:169], v[58:61]
	v_mfma_f32_16x16x32_bf16 v[46:49], v[142:145], v[174:177], v[46:49]
	v_mfma_f32_16x16x32_bf16 v[54:57], v[134:137], v[174:177], v[54:57]
	v_mfma_f32_16x16x32_bf16 v[38:41], v[134:137], v[182:185], v[38:41]
	v_mfma_f32_16x16x32_bf16 v[30:33], v[142:145], v[182:185], v[30:33]
	v_mfma_f32_16x16x32_bf16 v[14:17], v[142:145], v[212:215], v[14:17]
	v_mfma_f32_16x16x32_bf16 v[22:25], v[134:137], v[212:215], v[22:25]
	v_mfma_f32_16x16x32_bf16 v[50:53], v[146:149], v[162:165], v[50:53]
	v_mfma_f32_16x16x32_bf16 v[42:45], v[154:157], v[162:165], v[42:45]
	v_mfma_f32_16x16x32_bf16 v[26:29], v[154:157], v[170:173], v[26:29]
	v_mfma_f32_16x16x32_bf16 v[34:37], v[146:149], v[170:173], v[34:37]
	v_mfma_f32_16x16x32_bf16 v[18:21], v[146:149], v[178:181], v[18:21]
	v_mfma_f32_16x16x32_bf16 v[10:13], v[154:157], v[178:181], v[10:13]
	v_mfma_f32_16x16x32_bf16 v[2:5], v[154:157], v[186:189], v[2:5]
	v_mfma_f32_16x16x32_bf16 v[6:9], v[146:149], v[186:189], v[6:9]
	v_mfma_f32_16x16x32_bf16 v[50:53], v[150:153], v[166:169], v[50:53]
	v_mfma_f32_16x16x32_bf16 v[42:45], v[158:161], v[166:169], v[42:45]
	v_mfma_f32_16x16x32_bf16 v[26:29], v[158:161], v[174:177], v[26:29]
	v_mfma_f32_16x16x32_bf16 v[34:37], v[150:153], v[174:177], v[34:37]
	v_mfma_f32_16x16x32_bf16 v[18:21], v[150:153], v[182:185], v[18:21]
	v_mfma_f32_16x16x32_bf16 v[10:13], v[158:161], v[182:185], v[10:13]
	v_mfma_f32_16x16x32_bf16 v[2:5], v[158:161], v[212:215], v[2:5]
	v_mfma_f32_16x16x32_bf16 v[6:9], v[150:153], v[212:215], v[6:9]
	s_barrier
	ds_read_b128 v[130:133], v223
	ds_read_b128 v[134:137], v223 offset:1024
	ds_read_b128 v[138:141], v223 offset:2048
	ds_read_b128 v[142:145], v223 offset:3072
	ds_read_b128 v[146:149], v224
	ds_read_b128 v[150:153], v224 offset:1024
	ds_read_b128 v[154:157], v224 offset:2048
	ds_read_b128 v[158:161], v224 offset:3072
	s_add_i32 s87, s87, 0x80000
	s_mov_b32 m0, s74
	ds_read_b128 v[162:165], v222 offset:32768
	ds_read_b128 v[166:169], v222 offset:33792
	ds_read_b128 v[170:173], v222 offset:34816
	ds_read_b128 v[174:177], v222 offset:35840
	ds_read_b128 v[178:181], v222 offset:36864
	ds_read_b128 v[182:185], v222 offset:37888
	ds_read_b128 v[186:189], v222 offset:38912
	ds_read_b128 v[212:215], v222 offset:39936
	buffer_load_dwordx4 v1, s[40:43], s87 offen lds
	s_mov_b32 m0, s75
	s_nop 0
	buffer_load_dwordx4 v216, s[40:43], s87 offen lds
	s_waitcnt vmcnt(8)
	s_waitcnt lgkmcnt(0)
	s_barrier
	v_mfma_f32_16x16x32_bf16 v[126:129], v[130:133], v[162:165], v[126:129]
	v_mfma_f32_16x16x32_bf16 v[122:125], v[138:141], v[162:165], v[122:125]
	v_mfma_f32_16x16x32_bf16 v[106:109], v[138:141], v[170:173], v[106:109]
	v_mfma_f32_16x16x32_bf16 v[114:117], v[130:133], v[170:173], v[114:117]
	v_mfma_f32_16x16x32_bf16 v[102:105], v[130:133], v[178:181], v[102:105]
	v_mfma_f32_16x16x32_bf16 v[94:97], v[138:141], v[178:181], v[94:97]
	v_mfma_f32_16x16x32_bf16 v[78:81], v[138:141], v[186:189], v[78:81]
	v_mfma_f32_16x16x32_bf16 v[86:89], v[130:133], v[186:189], v[86:89]
	v_mfma_f32_16x16x32_bf16 v[126:129], v[134:137], v[166:169], v[126:129]
	v_mfma_f32_16x16x32_bf16 v[122:125], v[142:145], v[166:169], v[122:125]
	v_mfma_f32_16x16x32_bf16 v[106:109], v[142:145], v[174:177], v[106:109]
	v_mfma_f32_16x16x32_bf16 v[114:117], v[134:137], v[174:177], v[114:117]
	v_mfma_f32_16x16x32_bf16 v[102:105], v[134:137], v[182:185], v[102:105]
	v_mfma_f32_16x16x32_bf16 v[94:97], v[142:145], v[182:185], v[94:97]
	v_mfma_f32_16x16x32_bf16 v[78:81], v[142:145], v[212:215], v[78:81]
	v_mfma_f32_16x16x32_bf16 v[86:89], v[134:137], v[212:215], v[86:89]
	v_mfma_f32_16x16x32_bf16 v[118:121], v[146:149], v[162:165], v[118:121]
	v_mfma_f32_16x16x32_bf16 v[110:113], v[154:157], v[162:165], v[110:113]
	v_mfma_f32_16x16x32_bf16 v[90:93], v[154:157], v[170:173], v[90:93]
	v_mfma_f32_16x16x32_bf16 v[98:101], v[146:149], v[170:173], v[98:101]
	v_mfma_f32_16x16x32_bf16 v[82:85], v[146:149], v[178:181], v[82:85]
	v_mfma_f32_16x16x32_bf16 v[74:77], v[154:157], v[178:181], v[74:77]
	v_mfma_f32_16x16x32_bf16 v[66:69], v[154:157], v[186:189], v[66:69]
	v_mfma_f32_16x16x32_bf16 v[70:73], v[146:149], v[186:189], v[70:73]
	v_mfma_f32_16x16x32_bf16 v[118:121], v[150:153], v[166:169], v[118:121]
	v_mfma_f32_16x16x32_bf16 v[110:113], v[158:161], v[166:169], v[110:113]
	v_mfma_f32_16x16x32_bf16 v[90:93], v[158:161], v[174:177], v[90:93]
	v_mfma_f32_16x16x32_bf16 v[98:101], v[150:153], v[174:177], v[98:101]
	v_mfma_f32_16x16x32_bf16 v[82:85], v[150:153], v[182:185], v[82:85]
	v_mfma_f32_16x16x32_bf16 v[74:77], v[158:161], v[182:185], v[74:77]
	v_mfma_f32_16x16x32_bf16 v[66:69], v[158:161], v[212:215], v[66:69]
	v_mfma_f32_16x16x32_bf16 v[70:73], v[150:153], v[212:215], v[70:73]
	s_barrier
	s_mov_b32 m0, s79
	s_or_b32 s87, s86, 0x80
	ds_read_b128 v[162:165], v222 offset:49152
	ds_read_b128 v[166:169], v222 offset:50176
	ds_read_b128 v[170:173], v222 offset:51200
	ds_read_b128 v[174:177], v222 offset:52224
	ds_read_b128 v[178:181], v222 offset:53248
	ds_read_b128 v[182:185], v222 offset:54272
	ds_read_b128 v[186:189], v222 offset:55296
	ds_read_b128 v[212:215], v222 offset:56320
	buffer_load_dwordx4 v191, s[44:47], s87 offen lds
	s_mov_b32 m0, s80
	s_add_i32 s86, s86, 0x80080
	buffer_load_dwordx4 v217, s[44:47], s87 offen lds
	s_mov_b32 m0, s83
	s_nop 0
	buffer_load_dwordx4 v191, s[44:47], s86 offen lds
	s_mov_b32 m0, s92
	s_nop 0
	buffer_load_dwordx4 v217, s[44:47], s86 offen lds
	s_mov_b32 m0, s81
	s_nop 0
	buffer_load_dwordx4 v1, s[40:43], s85 offen lds
	s_mov_b32 m0, s82
	s_nop 0
	buffer_load_dwordx4 v216, s[40:43], s85 offen lds
	s_waitcnt vmcnt(8)
	s_waitcnt lgkmcnt(0)
	s_barrier
	v_mfma_f32_16x16x32_bf16 v[62:65], v[130:133], v[162:165], v[62:65]
	v_mfma_f32_16x16x32_bf16 v[58:61], v[138:141], v[162:165], v[58:61]
	v_mfma_f32_16x16x32_bf16 v[46:49], v[138:141], v[170:173], v[46:49]
	v_mfma_f32_16x16x32_bf16 v[54:57], v[130:133], v[170:173], v[54:57]
	v_mfma_f32_16x16x32_bf16 v[38:41], v[130:133], v[178:181], v[38:41]
	v_mfma_f32_16x16x32_bf16 v[30:33], v[138:141], v[178:181], v[30:33]
	v_mfma_f32_16x16x32_bf16 v[14:17], v[138:141], v[186:189], v[14:17]
	v_mfma_f32_16x16x32_bf16 v[22:25], v[130:133], v[186:189], v[22:25]
	v_mfma_f32_16x16x32_bf16 v[62:65], v[134:137], v[166:169], v[62:65]
	v_mfma_f32_16x16x32_bf16 v[58:61], v[142:145], v[166:169], v[58:61]
	v_mfma_f32_16x16x32_bf16 v[46:49], v[142:145], v[174:177], v[46:49]
	v_mfma_f32_16x16x32_bf16 v[54:57], v[134:137], v[174:177], v[54:57]
	v_mfma_f32_16x16x32_bf16 v[38:41], v[134:137], v[182:185], v[38:41]
	v_mfma_f32_16x16x32_bf16 v[30:33], v[142:145], v[182:185], v[30:33]
	v_mfma_f32_16x16x32_bf16 v[14:17], v[142:145], v[212:215], v[14:17]
	v_mfma_f32_16x16x32_bf16 v[22:25], v[134:137], v[212:215], v[22:25]
	v_mfma_f32_16x16x32_bf16 v[50:53], v[146:149], v[162:165], v[50:53]
	v_mfma_f32_16x16x32_bf16 v[42:45], v[154:157], v[162:165], v[42:45]
	v_mfma_f32_16x16x32_bf16 v[26:29], v[154:157], v[170:173], v[26:29]
	v_mfma_f32_16x16x32_bf16 v[34:37], v[146:149], v[170:173], v[34:37]
	v_mfma_f32_16x16x32_bf16 v[18:21], v[146:149], v[178:181], v[18:21]
	v_mfma_f32_16x16x32_bf16 v[10:13], v[154:157], v[178:181], v[10:13]
	v_mfma_f32_16x16x32_bf16 v[2:5], v[154:157], v[186:189], v[2:5]
	v_mfma_f32_16x16x32_bf16 v[6:9], v[146:149], v[186:189], v[6:9]
	v_mfma_f32_16x16x32_bf16 v[50:53], v[150:153], v[166:169], v[50:53]
	v_mfma_f32_16x16x32_bf16 v[42:45], v[158:161], v[166:169], v[42:45]
	v_mfma_f32_16x16x32_bf16 v[26:29], v[158:161], v[174:177], v[26:29]
	v_mfma_f32_16x16x32_bf16 v[34:37], v[150:153], v[174:177], v[34:37]
	v_mfma_f32_16x16x32_bf16 v[18:21], v[150:153], v[182:185], v[18:21]
	v_mfma_f32_16x16x32_bf16 v[10:13], v[158:161], v[182:185], v[10:13]
	v_mfma_f32_16x16x32_bf16 v[2:5], v[158:161], v[212:215], v[2:5]
	v_mfma_f32_16x16x32_bf16 v[6:9], v[150:153], v[212:215], v[6:9]
	s_barrier
	s_add_i32 s84, s84, 2
	s_addk_i32 s64, 0x100
	s_addk_i32 s65, 0x100
	s_cmp_gt_u32 s84, 29
	s_cbranch_scc0 .LBB0_114
	s_and_b64 vcc, exec, s[56:57]
	s_cbranch_vccz .LBB0_127
	s_barrier
	s_cmp_gt_i32 s61, 23
	s_mov_b64 s[46:47], -1
	s_cbranch_scc1 .LBB0_128

.LBB0_563:
	v_add_u32_e32 v3, 0x10000, v209
	ds_read_b128 v[140:143], v3
	ds_read_b128 v[144:147], v3 offset:1024
	ds_read_b128 v[148:151], v3 offset:2048
	ds_read_b128 v[152:155], v3 offset:3072
	v_add_u32_e32 v3, 0x14000, v209
	ds_read_b128 v[156:159], v3
	ds_read_b128 v[160:163], v3 offset:1024
	ds_read_b128 v[164:167], v3 offset:2048
	ds_read_b128 v[168:171], v3 offset:3072
	s_add_i32 s10, s57, 0xfff80080
	s_cmp_eq_u32 s59, 12
	s_cselect_b32 s62, s2, s10
	s_cselect_b32 s61, s3, s58
	s_add_i32 s60, s62, 0x80
	s_mov_b32 m0, s44
	ds_read_b128 v[172:175], v210
	ds_read_b128 v[176:179], v210 offset:1024
	ds_read_b128 v[180:183], v210 offset:2048
	ds_read_b128 v[184:187], v210 offset:3072
	ds_read_b128 v[188:191], v210 offset:4096
	ds_read_b128 v[192:195], v210 offset:5120
	ds_read_b128 v[196:199], v210 offset:6144
	ds_read_b128 v[200:203], v210 offset:7168
	buffer_load_dwordx4 v1, s[4:7], s57 offen lds
	s_mov_b32 m0, s45
	s_nop 0
	buffer_load_dwordx4 v206, s[4:7], s57 offen lds
	s_waitcnt vmcnt(8)
	s_waitcnt lgkmcnt(0)
	s_barrier
	v_mfma_f32_16x16x32_bf16 v[130:133], v[140:143], v[172:175], v[130:133]
	v_mfma_f32_16x16x32_bf16 v[126:129], v[148:151], v[172:175], v[126:129]
	v_mfma_f32_16x16x32_bf16 v[122:125], v[140:143], v[180:183], v[122:125]
	v_mfma_f32_16x16x32_bf16 v[118:121], v[148:151], v[180:183], v[118:121]
	v_mfma_f32_16x16x32_bf16 v[114:117], v[140:143], v[188:191], v[114:117]
	v_mfma_f32_16x16x32_bf16 v[110:113], v[148:151], v[188:191], v[110:113]
	v_mfma_f32_16x16x32_bf16 v[106:109], v[140:143], v[196:199], v[106:109]
	v_mfma_f32_16x16x32_bf16 v[102:105], v[148:151], v[196:199], v[102:105]
	v_mfma_f32_16x16x32_bf16 v[130:133], v[144:147], v[176:179], v[130:133]
	v_mfma_f32_16x16x32_bf16 v[126:129], v[152:155], v[176:179], v[126:129]
	v_mfma_f32_16x16x32_bf16 v[122:125], v[144:147], v[184:187], v[122:125]
	v_mfma_f32_16x16x32_bf16 v[118:121], v[152:155], v[184:187], v[118:121]
	v_mfma_f32_16x16x32_bf16 v[114:117], v[144:147], v[192:195], v[114:117]
	v_mfma_f32_16x16x32_bf16 v[110:113], v[152:155], v[192:195], v[110:113]
	v_mfma_f32_16x16x32_bf16 v[106:109], v[144:147], v[200:203], v[106:109]
	v_mfma_f32_16x16x32_bf16 v[102:105], v[152:155], v[200:203], v[102:105]
	v_mfma_f32_16x16x32_bf16 v[98:101], v[156:159], v[172:175], v[98:101]
	v_mfma_f32_16x16x32_bf16 v[94:97], v[164:167], v[172:175], v[94:97]
	v_mfma_f32_16x16x32_bf16 v[90:93], v[156:159], v[180:183], v[90:93]
	v_mfma_f32_16x16x32_bf16 v[86:89], v[164:167], v[180:183], v[86:89]
	v_mfma_f32_16x16x32_bf16 v[82:85], v[156:159], v[188:191], v[82:85]
	v_mfma_f32_16x16x32_bf16 v[78:81], v[164:167], v[188:191], v[78:81]
	v_mfma_f32_16x16x32_bf16 v[74:77], v[156:159], v[196:199], v[74:77]
	v_mfma_f32_16x16x32_bf16 v[70:73], v[164:167], v[196:199], v[70:73]
	v_mfma_f32_16x16x32_bf16 v[98:101], v[160:163], v[176:179], v[98:101]
	v_mfma_f32_16x16x32_bf16 v[94:97], v[168:171], v[176:179], v[94:97]
	v_mfma_f32_16x16x32_bf16 v[90:93], v[160:163], v[184:187], v[90:93]
	v_mfma_f32_16x16x32_bf16 v[86:89], v[168:171], v[184:187], v[86:89]
	v_mfma_f32_16x16x32_bf16 v[82:85], v[160:163], v[192:195], v[82:85]
	v_mfma_f32_16x16x32_bf16 v[78:81], v[168:171], v[192:195], v[78:81]
	v_mfma_f32_16x16x32_bf16 v[74:77], v[160:163], v[200:203], v[74:77]
	v_mfma_f32_16x16x32_bf16 v[70:73], v[168:171], v[200:203], v[70:73]
	s_barrier
	s_mov_b32 m0, s28
	s_mov_b32 s10, s6
	s_mov_b32 s11, s7
	ds_read_b128 v[172:175], v210 offset:16384
	ds_read_b128 v[176:179], v210 offset:17408
	ds_read_b128 v[180:183], v210 offset:18432
	ds_read_b128 v[184:187], v210 offset:19456
	ds_read_b128 v[188:191], v210 offset:20480
	ds_read_b128 v[192:195], v210 offset:21504
	ds_read_b128 v[196:199], v210 offset:22528
	ds_read_b128 v[200:203], v210 offset:23552
	buffer_load_dwordx4 v135, s[8:11], s61 offen lds
	s_mov_b32 m0, s29
	s_add_i32 s63, s61, 0x80000
	buffer_load_dwordx4 v207, s[8:11], s61 offen lds
	s_mov_b32 m0, s30
	s_nop 0
	buffer_load_dwordx4 v135, s[8:11], s63 offen lds
	s_mov_b32 m0, s31
	s_nop 0
	buffer_load_dwordx4 v207, s[8:11], s63 offen lds
	s_mov_b32 m0, s27
	s_nop 0
	buffer_load_dwordx4 v1, s[4:7], s62 offen lds
	s_mov_b32 m0, s33
	s_nop 0
	buffer_load_dwordx4 v206, s[4:7], s62 offen lds
	s_waitcnt vmcnt(8)
	s_waitcnt lgkmcnt(0)
	s_barrier
	v_mfma_f32_16x16x32_bf16 v[66:69], v[140:143], v[172:175], v[66:69]
	v_mfma_f32_16x16x32_bf16 v[62:65], v[148:151], v[172:175], v[62:65]
	v_mfma_f32_16x16x32_bf16 v[58:61], v[140:143], v[180:183], v[58:61]
	v_mfma_f32_16x16x32_bf16 v[54:57], v[148:151], v[180:183], v[54:57]
	v_mfma_f32_16x16x32_bf16 v[50:53], v[140:143], v[188:191], v[50:53]
	v_mfma_f32_16x16x32_bf16 v[46:49], v[148:151], v[188:191], v[46:49]
	v_mfma_f32_16x16x32_bf16 v[42:45], v[140:143], v[196:199], v[42:45]
	v_mfma_f32_16x16x32_bf16 v[38:41], v[148:151], v[196:199], v[38:41]
	v_mfma_f32_16x16x32_bf16 v[66:69], v[144:147], v[176:179], v[66:69]
	v_mfma_f32_16x16x32_bf16 v[62:65], v[152:155], v[176:179], v[62:65]
	v_mfma_f32_16x16x32_bf16 v[58:61], v[144:147], v[184:187], v[58:61]
	v_mfma_f32_16x16x32_bf16 v[54:57], v[152:155], v[184:187], v[54:57]
	v_mfma_f32_16x16x32_bf16 v[50:53], v[144:147], v[192:195], v[50:53]
	v_mfma_f32_16x16x32_bf16 v[46:49], v[152:155], v[192:195], v[46:49]
	v_mfma_f32_16x16x32_bf16 v[42:45], v[144:147], v[200:203], v[42:45]
	v_mfma_f32_16x16x32_bf16 v[38:41], v[152:155], v[200:203], v[38:41]
	v_mfma_f32_16x16x32_bf16 v[34:37], v[156:159], v[172:175], v[34:37]
	v_mfma_f32_16x16x32_bf16 v[30:33], v[164:167], v[172:175], v[30:33]
	v_mfma_f32_16x16x32_bf16 v[26:29], v[156:159], v[180:183], v[26:29]
	v_mfma_f32_16x16x32_bf16 v[22:25], v[164:167], v[180:183], v[22:25]
	v_mfma_f32_16x16x32_bf16 v[18:21], v[156:159], v[188:191], v[18:21]
	v_mfma_f32_16x16x32_bf16 v[14:17], v[164:167], v[188:191], v[14:17]
	v_mfma_f32_16x16x32_bf16 v[10:13], v[156:159], v[196:199], v[10:13]
	v_mfma_f32_16x16x32_bf16 v[4:7], v[164:167], v[196:199], v[6:9]
	v_mfma_f32_16x16x32_bf16 v[34:37], v[160:163], v[176:179], v[34:37]
	v_mfma_f32_16x16x32_bf16 v[30:33], v[168:171], v[176:179], v[30:33]
	v_mfma_f32_16x16x32_bf16 v[26:29], v[160:163], v[184:187], v[26:29]
	v_mfma_f32_16x16x32_bf16 v[22:25], v[168:171], v[184:187], v[22:25]
	v_mfma_f32_16x16x32_bf16 v[18:21], v[160:163], v[192:195], v[18:21]
	v_mfma_f32_16x16x32_bf16 v[14:17], v[168:171], v[192:195], v[14:17]
	v_mfma_f32_16x16x32_bf16 v[10:13], v[160:163], v[200:203], v[10:13]
	v_mfma_f32_16x16x32_bf16 v[4:7], v[168:171], v[200:203], v[4:7]
	s_barrier
	v_add_u32_e32 v3, 0x18000, v209
	ds_read_b128 v[140:143], v3
	ds_read_b128 v[144:147], v3 offset:1024
	ds_read_b128 v[148:151], v3 offset:2048
	ds_read_b128 v[152:155], v3 offset:3072
	v_add_u32_e32 v3, 0x1c000, v209
	ds_read_b128 v[156:159], v3
	ds_read_b128 v[160:163], v3 offset:1024
	ds_read_b128 v[164:167], v3 offset:2048
	ds_read_b128 v[168:171], v3 offset:3072
	s_add_i32 s62, s62, 0x80000
	s_mov_b32 m0, s34
	ds_read_b128 v[172:175], v210 offset:32768
	ds_read_b128 v[176:179], v210 offset:33792
	ds_read_b128 v[180:183], v210 offset:34816
	ds_read_b128 v[184:187], v210 offset:35840
	ds_read_b128 v[188:191], v210 offset:36864
	ds_read_b128 v[192:195], v210 offset:37888
	ds_read_b128 v[196:199], v210 offset:38912
	ds_read_b128 v[200:203], v210 offset:39936
	buffer_load_dwordx4 v1, s[4:7], s62 offen lds
	s_mov_b32 m0, s35
	s_nop 0
	buffer_load_dwordx4 v206, s[4:7], s62 offen lds
	s_waitcnt vmcnt(8)
	s_waitcnt lgkmcnt(0)
	s_barrier
	v_mfma_f32_16x16x32_bf16 v[130:133], v[140:143], v[172:175], v[130:133]
	v_mfma_f32_16x16x32_bf16 v[126:129], v[148:151], v[172:175], v[126:129]
	v_mfma_f32_16x16x32_bf16 v[122:125], v[140:143], v[180:183], v[122:125]
	v_mfma_f32_16x16x32_bf16 v[118:121], v[148:151], v[180:183], v[118:121]
	v_mfma_f32_16x16x32_bf16 v[114:117], v[140:143], v[188:191], v[114:117]
	v_mfma_f32_16x16x32_bf16 v[110:113], v[148:151], v[188:191], v[110:113]
	v_mfma_f32_16x16x32_bf16 v[106:109], v[140:143], v[196:199], v[106:109]
	v_mfma_f32_16x16x32_bf16 v[102:105], v[148:151], v[196:199], v[102:105]
	v_mfma_f32_16x16x32_bf16 v[130:133], v[144:147], v[176:179], v[130:133]
	v_mfma_f32_16x16x32_bf16 v[126:129], v[152:155], v[176:179], v[126:129]
	v_mfma_f32_16x16x32_bf16 v[122:125], v[144:147], v[184:187], v[122:125]
	v_mfma_f32_16x16x32_bf16 v[118:121], v[152:155], v[184:187], v[118:121]
	v_mfma_f32_16x16x32_bf16 v[114:117], v[144:147], v[192:195], v[114:117]
	v_mfma_f32_16x16x32_bf16 v[110:113], v[152:155], v[192:195], v[110:113]
	v_mfma_f32_16x16x32_bf16 v[106:109], v[144:147], v[200:203], v[106:109]
	v_mfma_f32_16x16x32_bf16 v[102:105], v[152:155], v[200:203], v[102:105]
	v_mfma_f32_16x16x32_bf16 v[98:101], v[156:159], v[172:175], v[98:101]
	v_mfma_f32_16x16x32_bf16 v[94:97], v[164:167], v[172:175], v[94:97]
	v_mfma_f32_16x16x32_bf16 v[90:93], v[156:159], v[180:183], v[90:93]
	v_mfma_f32_16x16x32_bf16 v[86:89], v[164:167], v[180:183], v[86:89]
	v_mfma_f32_16x16x32_bf16 v[82:85], v[156:159], v[188:191], v[82:85]
	v_mfma_f32_16x16x32_bf16 v[78:81], v[164:167], v[188:191], v[78:81]
	v_mfma_f32_16x16x32_bf16 v[74:77], v[156:159], v[196:199], v[74:77]
	v_mfma_f32_16x16x32_bf16 v[70:73], v[164:167], v[196:199], v[70:73]
	v_mfma_f32_16x16x32_bf16 v[98:101], v[160:163], v[176:179], v[98:101]
	v_mfma_f32_16x16x32_bf16 v[94:97], v[168:171], v[176:179], v[94:97]
	v_mfma_f32_16x16x32_bf16 v[90:93], v[160:163], v[184:187], v[90:93]
	v_mfma_f32_16x16x32_bf16 v[86:89], v[168:171], v[184:187], v[86:89]
	v_mfma_f32_16x16x32_bf16 v[82:85], v[160:163], v[192:195], v[82:85]
	v_mfma_f32_16x16x32_bf16 v[78:81], v[168:171], v[192:195], v[78:81]
	v_mfma_f32_16x16x32_bf16 v[74:77], v[160:163], v[200:203], v[74:77]
	v_mfma_f32_16x16x32_bf16 v[70:73], v[168:171], v[200:203], v[70:73]
	s_barrier
	s_mov_b32 m0, s38
	s_add_i32 s62, s61, 0x80
	ds_read_b128 v[172:175], v210 offset:49152
	ds_read_b128 v[176:179], v210 offset:50176
	ds_read_b128 v[180:183], v210 offset:51200
	ds_read_b128 v[184:187], v210 offset:52224
	ds_read_b128 v[188:191], v210 offset:53248
	ds_read_b128 v[192:195], v210 offset:54272
	ds_read_b128 v[196:199], v210 offset:55296
	ds_read_b128 v[200:203], v210 offset:56320
	buffer_load_dwordx4 v135, s[8:11], s62 offen lds
	s_mov_b32 m0, s39
	s_add_i32 s61, s61, 0x80080
	buffer_load_dwordx4 v207, s[8:11], s62 offen lds
	s_mov_b32 m0, s42
	s_nop 0
	buffer_load_dwordx4 v135, s[8:11], s61 offen lds
	s_mov_b32 m0, s43
	s_nop 0
	buffer_load_dwordx4 v207, s[8:11], s61 offen lds
	s_mov_b32 m0, s40
	s_nop 0
	buffer_load_dwordx4 v1, s[4:7], s60 offen lds
	s_mov_b32 m0, s41
	s_nop 0
	buffer_load_dwordx4 v206, s[4:7], s60 offen lds
	s_waitcnt vmcnt(8)
	s_waitcnt lgkmcnt(0)
	s_barrier
	v_mfma_f32_16x16x32_bf16 v[66:69], v[140:143], v[172:175], v[66:69]
	v_mfma_f32_16x16x32_bf16 v[62:65], v[148:151], v[172:175], v[62:65]
	v_mfma_f32_16x16x32_bf16 v[58:61], v[140:143], v[180:183], v[58:61]
	v_mfma_f32_16x16x32_bf16 v[54:57], v[148:151], v[180:183], v[54:57]
	v_mfma_f32_16x16x32_bf16 v[50:53], v[140:143], v[188:191], v[50:53]
	v_mfma_f32_16x16x32_bf16 v[46:49], v[148:151], v[188:191], v[46:49]
	v_mfma_f32_16x16x32_bf16 v[42:45], v[140:143], v[196:199], v[42:45]
	v_mfma_f32_16x16x32_bf16 v[38:41], v[148:151], v[196:199], v[38:41]
	v_mfma_f32_16x16x32_bf16 v[66:69], v[144:147], v[176:179], v[66:69]
	v_mfma_f32_16x16x32_bf16 v[62:65], v[152:155], v[176:179], v[62:65]
	v_mfma_f32_16x16x32_bf16 v[58:61], v[144:147], v[184:187], v[58:61]
	v_mfma_f32_16x16x32_bf16 v[54:57], v[152:155], v[184:187], v[54:57]
	v_mfma_f32_16x16x32_bf16 v[50:53], v[144:147], v[192:195], v[50:53]
	v_mfma_f32_16x16x32_bf16 v[46:49], v[152:155], v[192:195], v[46:49]
	v_mfma_f32_16x16x32_bf16 v[42:45], v[144:147], v[200:203], v[42:45]
	v_mfma_f32_16x16x32_bf16 v[38:41], v[152:155], v[200:203], v[38:41]
	v_mfma_f32_16x16x32_bf16 v[34:37], v[156:159], v[172:175], v[34:37]
	v_mfma_f32_16x16x32_bf16 v[30:33], v[164:167], v[172:175], v[30:33]
	v_mfma_f32_16x16x32_bf16 v[26:29], v[156:159], v[180:183], v[26:29]
	v_mfma_f32_16x16x32_bf16 v[22:25], v[164:167], v[180:183], v[22:25]
	v_mfma_f32_16x16x32_bf16 v[18:21], v[156:159], v[188:191], v[18:21]
	v_mfma_f32_16x16x32_bf16 v[14:17], v[164:167], v[188:191], v[14:17]
	v_mfma_f32_16x16x32_bf16 v[8:11], v[156:159], v[196:199], v[10:13]
	v_mfma_f32_16x16x32_bf16 v[4:7], v[164:167], v[196:199], v[4:7]
	v_mfma_f32_16x16x32_bf16 v[34:37], v[160:163], v[176:179], v[34:37]
	v_mfma_f32_16x16x32_bf16 v[30:33], v[168:171], v[176:179], v[30:33]
	v_mfma_f32_16x16x32_bf16 v[26:29], v[160:163], v[184:187], v[26:29]
	v_mfma_f32_16x16x32_bf16 v[22:25], v[168:171], v[184:187], v[22:25]
	v_mfma_f32_16x16x32_bf16 v[18:21], v[160:163], v[192:195], v[18:21]
	v_mfma_f32_16x16x32_bf16 v[14:17], v[168:171], v[192:195], v[14:17]
	v_mfma_f32_16x16x32_bf16 v[10:13], v[160:163], v[200:203], v[8:11]
	v_mfma_f32_16x16x32_bf16 v[6:9], v[168:171], v[200:203], v[4:7]
	s_barrier
	s_add_i32 s59, s59, 2
	s_addk_i32 s57, 0x100
	s_addk_i32 s58, 0x100
	s_cmp_gt_u32 s59, 13
	s_cbranch_scc0 .LBB0_563
	s_and_b64 vcc, exec, s[20:21]
	s_cbranch_vccz .LBB0_566
	s_barrier

.LBB0_686:
	v_add_u32_e32 v152, 0x10000, v138
	v_add_u32_e32 v168, 0x14000, v138
	ds_read_b128 v[140:143], v152
	ds_read_b128 v[144:147], v152 offset:1024
	ds_read_b128 v[148:151], v152 offset:2048
	ds_read_b128 v[152:155], v152 offset:3072
	ds_read_b128 v[156:159], v168
	ds_read_b128 v[160:163], v168 offset:1024
	ds_read_b128 v[164:167], v168 offset:2048
	ds_read_b128 v[168:171], v168 offset:3072
	s_add_i32 s10, s33, s52
	s_add_i32 s53, s27, s52
	s_add_i32 s11, s10, 0x1000
	s_addk_i32 s53, 0x1000
	s_cmp_eq_u32 s52, 0
	s_cselect_b32 s55, s49, s11
	s_cselect_b32 s54, s50, s53
	s_or_b32 s53, s55, 0x80
	s_add_i32 s10, s10, 0x80f80
	s_mov_b32 m0, s43
	ds_read_b128 v[172:175], v139
	ds_read_b128 v[176:179], v139 offset:1024
	ds_read_b128 v[180:183], v139 offset:2048
	ds_read_b128 v[184:187], v139 offset:3072
	ds_read_b128 v[188:191], v139 offset:4096
	ds_read_b128 v[192:195], v139 offset:5120
	ds_read_b128 v[196:199], v139 offset:6144
	ds_read_b128 v[200:203], v139 offset:7168
	buffer_load_dwordx4 v134, s[4:7], s10 offen lds
	s_mov_b32 m0, s44
	s_nop 0
	buffer_load_dwordx4 v136, s[4:7], s10 offen lds
	s_waitcnt vmcnt(8)
	s_waitcnt lgkmcnt(0)
	s_barrier
	v_mfma_f32_16x16x32_bf16 v[126:129], v[140:143], v[172:175], v[126:129]
	v_mfma_f32_16x16x32_bf16 v[122:125], v[148:151], v[172:175], v[122:125]
	v_mfma_f32_16x16x32_bf16 v[106:109], v[148:151], v[180:183], v[106:109]
	v_mfma_f32_16x16x32_bf16 v[110:113], v[140:143], v[180:183], v[110:113]
	v_mfma_f32_16x16x32_bf16 v[98:101], v[140:143], v[188:191], v[98:101]
	v_mfma_f32_16x16x32_bf16 v[90:93], v[148:151], v[188:191], v[90:93]
	v_mfma_f32_16x16x32_bf16 v[74:77], v[148:151], v[196:199], v[74:77]
	v_mfma_f32_16x16x32_bf16 v[82:85], v[140:143], v[196:199], v[82:85]
	v_mfma_f32_16x16x32_bf16 v[126:129], v[144:147], v[176:179], v[126:129]
	v_mfma_f32_16x16x32_bf16 v[122:125], v[152:155], v[176:179], v[122:125]
	v_mfma_f32_16x16x32_bf16 v[106:109], v[152:155], v[184:187], v[106:109]
	v_mfma_f32_16x16x32_bf16 v[110:113], v[144:147], v[184:187], v[110:113]
	v_mfma_f32_16x16x32_bf16 v[98:101], v[144:147], v[192:195], v[98:101]
	v_mfma_f32_16x16x32_bf16 v[90:93], v[152:155], v[192:195], v[90:93]
	v_mfma_f32_16x16x32_bf16 v[74:77], v[152:155], v[200:203], v[74:77]
	v_mfma_f32_16x16x32_bf16 v[82:85], v[144:147], v[200:203], v[82:85]
	v_mfma_f32_16x16x32_bf16 v[118:121], v[156:159], v[172:175], v[118:121]
	v_mfma_f32_16x16x32_bf16 v[114:117], v[164:167], v[172:175], v[114:117]
	v_mfma_f32_16x16x32_bf16 v[94:97], v[164:167], v[180:183], v[94:97]
	v_mfma_f32_16x16x32_bf16 v[102:105], v[156:159], v[180:183], v[102:105]
	v_mfma_f32_16x16x32_bf16 v[86:89], v[156:159], v[188:191], v[86:89]
	v_mfma_f32_16x16x32_bf16 v[78:81], v[164:167], v[188:191], v[78:81]
	v_mfma_f32_16x16x32_bf16 v[66:69], v[164:167], v[196:199], v[66:69]
	v_mfma_f32_16x16x32_bf16 v[70:73], v[156:159], v[196:199], v[70:73]
	v_mfma_f32_16x16x32_bf16 v[118:121], v[160:163], v[176:179], v[118:121]
	v_mfma_f32_16x16x32_bf16 v[114:117], v[168:171], v[176:179], v[114:117]
	v_mfma_f32_16x16x32_bf16 v[94:97], v[168:171], v[184:187], v[94:97]
	v_mfma_f32_16x16x32_bf16 v[102:105], v[160:163], v[184:187], v[102:105]
	v_mfma_f32_16x16x32_bf16 v[86:89], v[160:163], v[192:195], v[86:89]
	v_mfma_f32_16x16x32_bf16 v[78:81], v[168:171], v[192:195], v[78:81]
	v_mfma_f32_16x16x32_bf16 v[66:69], v[168:171], v[200:203], v[66:69]
	v_mfma_f32_16x16x32_bf16 v[70:73], v[160:163], v[200:203], v[70:73]
	s_barrier
	s_mov_b32 m0, s26
	s_mov_b32 s10, s6
	s_mov_b32 s11, s7
	ds_read_b128 v[172:175], v139 offset:16384
	ds_read_b128 v[176:179], v139 offset:17408
	ds_read_b128 v[180:183], v139 offset:18432
	ds_read_b128 v[184:187], v139 offset:19456
	ds_read_b128 v[188:191], v139 offset:20480
	ds_read_b128 v[192:195], v139 offset:21504
	ds_read_b128 v[196:199], v139 offset:22528
	ds_read_b128 v[200:203], v139 offset:23552
	buffer_load_dwordx4 v135, s[8:11], s54 offen lds
	s_mov_b32 m0, s28
	s_add_i32 s56, s54, 0x80000
	buffer_load_dwordx4 v137, s[8:11], s54 offen lds
	s_mov_b32 m0, s29
	s_nop 0
	buffer_load_dwordx4 v135, s[8:11], s56 offen lds
	s_mov_b32 m0, s30
	s_nop 0
	buffer_load_dwordx4 v137, s[8:11], s56 offen lds
	s_mov_b32 m0, s25
	s_nop 0
	buffer_load_dwordx4 v134, s[4:7], s55 offen lds
	s_mov_b32 m0, s31
	s_nop 0
	buffer_load_dwordx4 v136, s[4:7], s55 offen lds
	s_waitcnt vmcnt(8)
	s_waitcnt lgkmcnt(0)
	s_barrier
	v_mfma_f32_16x16x32_bf16 v[62:65], v[140:143], v[172:175], v[62:65]
	v_mfma_f32_16x16x32_bf16 v[58:61], v[148:151], v[172:175], v[58:61]
	v_mfma_f32_16x16x32_bf16 v[42:45], v[148:151], v[180:183], v[42:45]
	v_mfma_f32_16x16x32_bf16 v[46:49], v[140:143], v[180:183], v[46:49]
	v_mfma_f32_16x16x32_bf16 v[30:33], v[140:143], v[188:191], v[30:33]
	v_mfma_f32_16x16x32_bf16 v[26:29], v[148:151], v[188:191], v[26:29]
	v_mfma_f32_16x16x32_bf16 v[10:13], v[148:151], v[196:199], v[10:13]
	v_mfma_f32_16x16x32_bf16 v[14:17], v[140:143], v[196:199], v[14:17]
	v_mfma_f32_16x16x32_bf16 v[62:65], v[144:147], v[176:179], v[62:65]
	v_mfma_f32_16x16x32_bf16 v[58:61], v[152:155], v[176:179], v[58:61]
	v_mfma_f32_16x16x32_bf16 v[42:45], v[152:155], v[184:187], v[42:45]
	v_mfma_f32_16x16x32_bf16 v[46:49], v[144:147], v[184:187], v[46:49]
	v_mfma_f32_16x16x32_bf16 v[30:33], v[144:147], v[192:195], v[30:33]
	v_mfma_f32_16x16x32_bf16 v[26:29], v[152:155], v[192:195], v[26:29]
	v_mfma_f32_16x16x32_bf16 v[10:13], v[152:155], v[200:203], v[10:13]
	v_mfma_f32_16x16x32_bf16 v[14:17], v[144:147], v[200:203], v[14:17]
	v_mfma_f32_16x16x32_bf16 v[54:57], v[156:159], v[172:175], v[54:57]
	v_mfma_f32_16x16x32_bf16 v[50:53], v[164:167], v[172:175], v[50:53]
	v_mfma_f32_16x16x32_bf16 v[34:37], v[164:167], v[180:183], v[34:37]
	v_mfma_f32_16x16x32_bf16 v[38:41], v[156:159], v[180:183], v[38:41]
	v_mfma_f32_16x16x32_bf16 v[22:25], v[156:159], v[188:191], v[22:25]
	v_mfma_f32_16x16x32_bf16 v[18:21], v[164:167], v[188:191], v[18:21]
	v_mfma_f32_16x16x32_bf16 v[2:5], v[164:167], v[196:199], v[2:5]
	v_mfma_f32_16x16x32_bf16 v[6:9], v[156:159], v[196:199], v[6:9]
	v_mfma_f32_16x16x32_bf16 v[54:57], v[160:163], v[176:179], v[54:57]
	v_mfma_f32_16x16x32_bf16 v[50:53], v[168:171], v[176:179], v[50:53]
	v_mfma_f32_16x16x32_bf16 v[34:37], v[168:171], v[184:187], v[34:37]
	v_mfma_f32_16x16x32_bf16 v[38:41], v[160:163], v[184:187], v[38:41]
	v_mfma_f32_16x16x32_bf16 v[22:25], v[160:163], v[192:195], v[22:25]
	v_mfma_f32_16x16x32_bf16 v[18:21], v[168:171], v[192:195], v[18:21]
	v_mfma_f32_16x16x32_bf16 v[2:5], v[168:171], v[200:203], v[2:5]
	v_mfma_f32_16x16x32_bf16 v[6:9], v[160:163], v[200:203], v[6:9]
	s_barrier
	v_add_u32_e32 v152, 0x18000, v138
	v_add_u32_e32 v168, 0x1c000, v138
	ds_read_b128 v[140:143], v152
	ds_read_b128 v[144:147], v152 offset:1024
	ds_read_b128 v[148:151], v152 offset:2048
	ds_read_b128 v[152:155], v152 offset:3072
	ds_read_b128 v[156:159], v168
	ds_read_b128 v[160:163], v168 offset:1024
	ds_read_b128 v[164:167], v168 offset:2048
	ds_read_b128 v[168:171], v168 offset:3072
	s_add_i32 s55, s55, 0x80000
	s_mov_b32 m0, s34
	ds_read_b128 v[172:175], v139 offset:32768
	ds_read_b128 v[176:179], v139 offset:33792
	ds_read_b128 v[180:183], v139 offset:34816
	ds_read_b128 v[184:187], v139 offset:35840
	ds_read_b128 v[188:191], v139 offset:36864
	ds_read_b128 v[192:195], v139 offset:37888
	ds_read_b128 v[196:199], v139 offset:38912
	ds_read_b128 v[200:203], v139 offset:39936
	buffer_load_dwordx4 v134, s[4:7], s55 offen lds
	s_mov_b32 m0, s35
	s_nop 0
	buffer_load_dwordx4 v136, s[4:7], s55 offen lds
	s_waitcnt vmcnt(8)
	s_waitcnt lgkmcnt(0)
	s_barrier
	v_mfma_f32_16x16x32_bf16 v[126:129], v[140:143], v[172:175], v[126:129]
	v_mfma_f32_16x16x32_bf16 v[122:125], v[148:151], v[172:175], v[122:125]
	v_mfma_f32_16x16x32_bf16 v[106:109], v[148:151], v[180:183], v[106:109]
	v_mfma_f32_16x16x32_bf16 v[110:113], v[140:143], v[180:183], v[110:113]
	v_mfma_f32_16x16x32_bf16 v[98:101], v[140:143], v[188:191], v[98:101]
	v_mfma_f32_16x16x32_bf16 v[90:93], v[148:151], v[188:191], v[90:93]
	v_mfma_f32_16x16x32_bf16 v[74:77], v[148:151], v[196:199], v[74:77]
	v_mfma_f32_16x16x32_bf16 v[82:85], v[140:143], v[196:199], v[82:85]
	v_mfma_f32_16x16x32_bf16 v[126:129], v[144:147], v[176:179], v[126:129]
	v_mfma_f32_16x16x32_bf16 v[122:125], v[152:155], v[176:179], v[122:125]
	v_mfma_f32_16x16x32_bf16 v[106:109], v[152:155], v[184:187], v[106:109]
	v_mfma_f32_16x16x32_bf16 v[110:113], v[144:147], v[184:187], v[110:113]
	v_mfma_f32_16x16x32_bf16 v[98:101], v[144:147], v[192:195], v[98:101]
	v_mfma_f32_16x16x32_bf16 v[90:93], v[152:155], v[192:195], v[90:93]
	v_mfma_f32_16x16x32_bf16 v[74:77], v[152:155], v[200:203], v[74:77]
	v_mfma_f32_16x16x32_bf16 v[82:85], v[144:147], v[200:203], v[82:85]
	v_mfma_f32_16x16x32_bf16 v[118:121], v[156:159], v[172:175], v[118:121]
	v_mfma_f32_16x16x32_bf16 v[114:117], v[164:167], v[172:175], v[114:117]
	v_mfma_f32_16x16x32_bf16 v[94:97], v[164:167], v[180:183], v[94:97]
	v_mfma_f32_16x16x32_bf16 v[102:105], v[156:159], v[180:183], v[102:105]
	v_mfma_f32_16x16x32_bf16 v[86:89], v[156:159], v[188:191], v[86:89]
	v_mfma_f32_16x16x32_bf16 v[78:81], v[164:167], v[188:191], v[78:81]
	v_mfma_f32_16x16x32_bf16 v[66:69], v[164:167], v[196:199], v[66:69]
	v_mfma_f32_16x16x32_bf16 v[70:73], v[156:159], v[196:199], v[70:73]
	v_mfma_f32_16x16x32_bf16 v[118:121], v[160:163], v[176:179], v[118:121]
	v_mfma_f32_16x16x32_bf16 v[114:117], v[168:171], v[176:179], v[114:117]
	v_mfma_f32_16x16x32_bf16 v[94:97], v[168:171], v[184:187], v[94:97]
	v_mfma_f32_16x16x32_bf16 v[102:105], v[160:163], v[184:187], v[102:105]
	v_mfma_f32_16x16x32_bf16 v[86:89], v[160:163], v[192:195], v[86:89]
	v_mfma_f32_16x16x32_bf16 v[78:81], v[168:171], v[192:195], v[78:81]
	v_mfma_f32_16x16x32_bf16 v[66:69], v[168:171], v[200:203], v[66:69]
	v_mfma_f32_16x16x32_bf16 v[70:73], v[160:163], v[200:203], v[70:73]
	s_barrier
	s_mov_b32 m0, s36
	s_or_b32 s55, s54, 0x80
	ds_read_b128 v[172:175], v139 offset:49152
	ds_read_b128 v[176:179], v139 offset:50176
	ds_read_b128 v[180:183], v139 offset:51200
	ds_read_b128 v[184:187], v139 offset:52224
	ds_read_b128 v[188:191], v139 offset:53248
	ds_read_b128 v[192:195], v139 offset:54272
	ds_read_b128 v[196:199], v139 offset:55296
	ds_read_b128 v[200:203], v139 offset:56320
	buffer_load_dwordx4 v135, s[8:11], s55 offen lds
	s_mov_b32 m0, s37
	s_add_i32 s54, s54, 0x80080
	buffer_load_dwordx4 v137, s[8:11], s55 offen lds
	s_mov_b32 m0, s41
	s_nop 0
	buffer_load_dwordx4 v135, s[8:11], s54 offen lds
	s_mov_b32 m0, s42
	s_nop 0
	buffer_load_dwordx4 v137, s[8:11], s54 offen lds
	s_mov_b32 m0, s38
	s_nop 0
	buffer_load_dwordx4 v134, s[4:7], s53 offen lds
	s_mov_b32 m0, s40
	s_nop 0
	buffer_load_dwordx4 v136, s[4:7], s53 offen lds
	s_waitcnt vmcnt(8)
	s_waitcnt lgkmcnt(0)
	s_barrier
	v_mfma_f32_16x16x32_bf16 v[62:65], v[140:143], v[172:175], v[62:65]
	v_mfma_f32_16x16x32_bf16 v[58:61], v[148:151], v[172:175], v[58:61]
	v_mfma_f32_16x16x32_bf16 v[42:45], v[148:151], v[180:183], v[42:45]
	v_mfma_f32_16x16x32_bf16 v[46:49], v[140:143], v[180:183], v[46:49]
	v_mfma_f32_16x16x32_bf16 v[30:33], v[140:143], v[188:191], v[30:33]
	v_mfma_f32_16x16x32_bf16 v[26:29], v[148:151], v[188:191], v[26:29]
	v_mfma_f32_16x16x32_bf16 v[10:13], v[148:151], v[196:199], v[10:13]
	v_mfma_f32_16x16x32_bf16 v[14:17], v[140:143], v[196:199], v[14:17]
	v_mfma_f32_16x16x32_bf16 v[62:65], v[144:147], v[176:179], v[62:65]
	v_mfma_f32_16x16x32_bf16 v[58:61], v[152:155], v[176:179], v[58:61]
	v_mfma_f32_16x16x32_bf16 v[42:45], v[152:155], v[184:187], v[42:45]
	v_mfma_f32_16x16x32_bf16 v[46:49], v[144:147], v[184:187], v[46:49]
	v_mfma_f32_16x16x32_bf16 v[30:33], v[144:147], v[192:195], v[30:33]
	v_mfma_f32_16x16x32_bf16 v[26:29], v[152:155], v[192:195], v[26:29]
	v_mfma_f32_16x16x32_bf16 v[10:13], v[152:155], v[200:203], v[10:13]
	v_mfma_f32_16x16x32_bf16 v[14:17], v[144:147], v[200:203], v[14:17]
	v_mfma_f32_16x16x32_bf16 v[54:57], v[156:159], v[172:175], v[54:57]
	v_mfma_f32_16x16x32_bf16 v[50:53], v[164:167], v[172:175], v[50:53]
	v_mfma_f32_16x16x32_bf16 v[34:37], v[164:167], v[180:183], v[34:37]
	v_mfma_f32_16x16x32_bf16 v[38:41], v[156:159], v[180:183], v[38:41]
	v_mfma_f32_16x16x32_bf16 v[22:25], v[156:159], v[188:191], v[22:25]
	v_mfma_f32_16x16x32_bf16 v[18:21], v[164:167], v[188:191], v[18:21]
	v_mfma_f32_16x16x32_bf16 v[2:5], v[164:167], v[196:199], v[2:5]
	v_mfma_f32_16x16x32_bf16 v[6:9], v[156:159], v[196:199], v[6:9]
	v_mfma_f32_16x16x32_bf16 v[54:57], v[160:163], v[176:179], v[54:57]
	v_mfma_f32_16x16x32_bf16 v[50:53], v[168:171], v[176:179], v[50:53]
	v_mfma_f32_16x16x32_bf16 v[34:37], v[168:171], v[184:187], v[34:37]
	v_mfma_f32_16x16x32_bf16 v[38:41], v[160:163], v[184:187], v[38:41]
	v_mfma_f32_16x16x32_bf16 v[22:25], v[160:163], v[192:195], v[22:25]
	v_mfma_f32_16x16x32_bf16 v[18:21], v[168:171], v[192:195], v[18:21]
	v_mfma_f32_16x16x32_bf16 v[2:5], v[168:171], v[200:203], v[2:5]
	v_mfma_f32_16x16x32_bf16 v[6:9], v[160:163], v[200:203], v[6:9]
	s_barrier
	s_add_i32 s51, s51, 2
	s_addk_i32 s52, 0x100
	s_cmp_gt_u32 s51, 29
	s_cbranch_scc0 .LBB0_686
	s_andn2_b64 vcc, exec, s[2:3]
	s_cbranch_vccnz .LBB0_678
	v_mov_b32_e32 v2, 0
	s_mov_b32 s14, s46
	s_mov_b32 s15, s47
	s_mov_b32 s27, s48
	s_mov_b32 s33, s13
	s_mov_b32 s45, s12
	v_mov_b32_e32 v3, v2
	v_mov_b32_e32 v4, v2
	v_mov_b32_e32 v5, v2
	v_mov_b32_e32 v6, v2
	v_mov_b32_e32 v7, v2
	v_mov_b32_e32 v8, v2
	v_mov_b32_e32 v9, v2
	v_mov_b32_e32 v18, v2
	v_mov_b32_e32 v19, v2
	v_mov_b32_e32 v20, v2
	v_mov_b32_e32 v21, v2
	v_mov_b32_e32 v22, v2
	v_mov_b32_e32 v23, v2
	v_mov_b32_e32 v24, v2
	v_mov_b32_e32 v25, v2
	v_mov_b32_e32 v34, v2
	v_mov_b32_e32 v35, v2
	v_mov_b32_e32 v36, v2
	v_mov_b32_e32 v37, v2
	v_mov_b32_e32 v38, v2
	v_mov_b32_e32 v39, v2
	v_mov_b32_e32 v40, v2
	v_mov_b32_e32 v41, v2
	v_mov_b32_e32 v50, v2
	v_mov_b32_e32 v51, v2
	v_mov_b32_e32 v52, v2
	v_mov_b32_e32 v53, v2
	v_mov_b32_e32 v54, v2
	v_mov_b32_e32 v55, v2
	v_mov_b32_e32 v56, v2
	v_mov_b32_e32 v57, v2
	v_mov_b32_e32 v10, v2
	v_mov_b32_e32 v11, v2
	v_mov_b32_e32 v12, v2
	v_mov_b32_e32 v13, v2
	v_mov_b32_e32 v14, v2
	v_mov_b32_e32 v15, v2
	v_mov_b32_e32 v16, v2
	v_mov_b32_e32 v17, v2
	v_mov_b32_e32 v26, v2
	v_mov_b32_e32 v27, v2
	v_mov_b32_e32 v28, v2
	v_mov_b32_e32 v29, v2
	v_mov_b32_e32 v30, v2
	v_mov_b32_e32 v31, v2
	v_mov_b32_e32 v32, v2
	v_mov_b32_e32 v33, v2
	v_mov_b32_e32 v42, v2
	v_mov_b32_e32 v43, v2
	v_mov_b32_e32 v44, v2
	v_mov_b32_e32 v45, v2
	v_mov_b32_e32 v46, v2
	v_mov_b32_e32 v47, v2
	v_mov_b32_e32 v48, v2
	v_mov_b32_e32 v49, v2
	v_mov_b32_e32 v58, v2
	v_mov_b32_e32 v59, v2
	v_mov_b32_e32 v60, v2
	v_mov_b32_e32 v61, v2
	v_mov_b32_e32 v62, v2
	v_mov_b32_e32 v63, v2
	v_mov_b32_e32 v64, v2
	v_mov_b32_e32 v65, v2
	v_mov_b32_e32 v66, v2
	v_mov_b32_e32 v67, v2
	v_mov_b32_e32 v68, v2
	v_mov_b32_e32 v69, v2
	v_mov_b32_e32 v70, v2
	v_mov_b32_e32 v71, v2
	v_mov_b32_e32 v72, v2
	v_mov_b32_e32 v73, v2
	v_mov_b32_e32 v78, v2
	v_mov_b32_e32 v79, v2
	v_mov_b32_e32 v80, v2
	v_mov_b32_e32 v81, v2
	v_mov_b32_e32 v86, v2
	v_mov_b32_e32 v87, v2
	v_mov_b32_e32 v88, v2
	v_mov_b32_e32 v89, v2
	v_mov_b32_e32 v94, v2
	v_mov_b32_e32 v95, v2
	v_mov_b32_e32 v96, v2
	v_mov_b32_e32 v97, v2
	v_mov_b32_e32 v102, v2
	v_mov_b32_e32 v103, v2
	v_mov_b32_e32 v104, v2
	v_mov_b32_e32 v105, v2
	v_mov_b32_e32 v114, v2
	v_mov_b32_e32 v115, v2
	v_mov_b32_e32 v116, v2
	v_mov_b32_e32 v117, v2
	v_mov_b32_e32 v118, v2
	v_mov_b32_e32 v119, v2
	v_mov_b32_e32 v120, v2
	v_mov_b32_e32 v121, v2
	v_mov_b32_e32 v74, v2
	v_mov_b32_e32 v75, v2
	v_mov_b32_e32 v76, v2
	v_mov_b32_e32 v77, v2
	v_mov_b32_e32 v82, v2
	v_mov_b32_e32 v83, v2
	v_mov_b32_e32 v84, v2
	v_mov_b32_e32 v85, v2
	v_mov_b32_e32 v90, v2
	v_mov_b32_e32 v91, v2
	v_mov_b32_e32 v92, v2
	v_mov_b32_e32 v93, v2
	v_mov_b32_e32 v98, v2
	v_mov_b32_e32 v99, v2
	v_mov_b32_e32 v100, v2
	v_mov_b32_e32 v101, v2
	v_mov_b32_e32 v106, v2
	v_mov_b32_e32 v107, v2
	v_mov_b32_e32 v108, v2
	v_mov_b32_e32 v109, v2
	v_mov_b32_e32 v110, v2
	v_mov_b32_e32 v111, v2
	v_mov_b32_e32 v112, v2
	v_mov_b32_e32 v113, v2
	v_mov_b32_e32 v122, v2
	v_mov_b32_e32 v123, v2
	v_mov_b32_e32 v124, v2
	v_mov_b32_e32 v125, v2
	v_mov_b32_e32 v126, v2
	v_mov_b32_e32 v127, v2
	v_mov_b32_e32 v128, v2
	v_mov_b32_e32 v129, v2
	s_branch .LBB0_678

.LBB0_907:
	v_add_u32_e32 v166, 0x10000, v179
	ds_read_b128 v[162:165], v166
	ds_read_b128 v[182:185], v166 offset:1024
	ds_read_b128 v[186:189], v166 offset:2048
	ds_read_b128 v[190:193], v166 offset:3072
	v_add_u32_e32 v166, 0x14000, v179
	ds_read_b128 v[194:197], v166
	ds_read_b128 v[198:201], v166 offset:1024
	ds_read_b128 v[202:205], v166 offset:2048
	ds_read_b128 v[206:209], v166 offset:3072
	s_add_i32 s10, s45, s64
	s_add_i32 s26, s40, s64
	s_add_i32 s11, s10, 0x1000
	s_addk_i32 s26, 0x1000
	s_cmp_eq_u32 s64, 0
	s_cselect_b32 s29, s62, s11
	s_cselect_b32 s27, s63, s26
	s_add_i32 s26, s29, 0x80
	s_add_i32 s28, s27, 0x80
	s_add_i32 s10, s10, 0x80f80
	s_mov_b32 m0, s55
	ds_read_b128 v[210:213], v180
	ds_read_b128 v[214:217], v180 offset:1024
	ds_read_b128 v[218:221], v180 offset:2048
	ds_read_b128 v[222:225], v180 offset:3072
	ds_read_b128 v[226:229], v180 offset:4096
	ds_read_b128 v[230:233], v180 offset:5120
	ds_read_b128 v[234:237], v180 offset:6144
	ds_read_b128 v[238:241], v180 offset:7168
	buffer_load_dwordx4 v1, s[4:7], s10 offen lds
	s_mov_b32 m0, s56
	s_nop 0
	buffer_load_dwordx4 v175, s[4:7], s10 offen lds
	s_waitcnt vmcnt(8)
	s_waitcnt lgkmcnt(0)
	s_barrier
	v_mfma_f32_16x16x32_bf16 v[126:129], v[162:165], v[210:213], v[126:129]
	v_mfma_f32_16x16x32_bf16 v[122:125], v[186:189], v[210:213], v[122:125]
	v_mfma_f32_16x16x32_bf16 v[114:117], v[186:189], v[218:221], v[114:117]
	v_mfma_f32_16x16x32_bf16 v[118:121], v[162:165], v[218:221], v[118:121]
	v_mfma_f32_16x16x32_bf16 v[110:113], v[162:165], v[226:229], v[110:113]
	v_mfma_f32_16x16x32_bf16 v[106:109], v[186:189], v[226:229], v[106:109]
	v_mfma_f32_16x16x32_bf16 v[98:101], v[186:189], v[234:237], v[98:101]
	v_mfma_f32_16x16x32_bf16 v[102:105], v[162:165], v[234:237], v[102:105]
	v_mfma_f32_16x16x32_bf16 v[126:129], v[182:185], v[214:217], v[126:129]
	v_mfma_f32_16x16x32_bf16 v[122:125], v[190:193], v[214:217], v[122:125]
	v_mfma_f32_16x16x32_bf16 v[114:117], v[190:193], v[222:225], v[114:117]
	v_mfma_f32_16x16x32_bf16 v[118:121], v[182:185], v[222:225], v[118:121]
	v_mfma_f32_16x16x32_bf16 v[110:113], v[182:185], v[230:233], v[110:113]
	v_mfma_f32_16x16x32_bf16 v[106:109], v[190:193], v[230:233], v[106:109]
	v_mfma_f32_16x16x32_bf16 v[98:101], v[190:193], v[238:241], v[98:101]
	v_mfma_f32_16x16x32_bf16 v[102:105], v[182:185], v[238:241], v[102:105]
	v_mfma_f32_16x16x32_bf16 v[94:97], v[194:197], v[210:213], v[94:97]
	v_mfma_f32_16x16x32_bf16 v[90:93], v[202:205], v[210:213], v[90:93]
	v_mfma_f32_16x16x32_bf16 v[82:85], v[202:205], v[218:221], v[82:85]
	v_mfma_f32_16x16x32_bf16 v[86:89], v[194:197], v[218:221], v[86:89]
	v_mfma_f32_16x16x32_bf16 v[78:81], v[194:197], v[226:229], v[78:81]
	v_mfma_f32_16x16x32_bf16 v[74:77], v[202:205], v[226:229], v[74:77]
	v_mfma_f32_16x16x32_bf16 v[66:69], v[202:205], v[234:237], v[66:69]
	v_mfma_f32_16x16x32_bf16 v[70:73], v[194:197], v[234:237], v[70:73]
	v_mfma_f32_16x16x32_bf16 v[94:97], v[198:201], v[214:217], v[94:97]
	v_mfma_f32_16x16x32_bf16 v[90:93], v[206:209], v[214:217], v[90:93]
	v_mfma_f32_16x16x32_bf16 v[82:85], v[206:209], v[222:225], v[82:85]
	v_mfma_f32_16x16x32_bf16 v[86:89], v[198:201], v[222:225], v[86:89]
	v_mfma_f32_16x16x32_bf16 v[78:81], v[198:201], v[230:233], v[78:81]
	v_mfma_f32_16x16x32_bf16 v[74:77], v[206:209], v[230:233], v[74:77]
	v_mfma_f32_16x16x32_bf16 v[66:69], v[206:209], v[238:241], v[66:69]
	v_mfma_f32_16x16x32_bf16 v[70:73], v[198:201], v[238:241], v[70:73]
	s_barrier
	s_mov_b32 m0, s37
	s_mov_b32 s10, s6
	s_mov_b32 s11, s7
	ds_read_b128 v[210:213], v180 offset:16384
	ds_read_b128 v[214:217], v180 offset:17408
	ds_read_b128 v[218:221], v180 offset:18432
	ds_read_b128 v[222:225], v180 offset:19456
	ds_read_b128 v[226:229], v180 offset:20480
	ds_read_b128 v[230:233], v180 offset:21504
	ds_read_b128 v[234:237], v180 offset:22528
	ds_read_b128 v[238:241], v180 offset:23552
	buffer_load_dwordx4 v174, s[8:11], s27 offen lds
	s_mov_b32 m0, s38
	s_add_i32 s66, s27, 0x80000
	buffer_load_dwordx4 v176, s[8:11], s27 offen lds
	s_mov_b32 m0, s39
	s_nop 0
	buffer_load_dwordx4 v174, s[8:11], s66 offen lds
	s_mov_b32 m0, s41
	s_nop 0
	buffer_load_dwordx4 v176, s[8:11], s66 offen lds
	s_mov_b32 m0, s36
	s_nop 0
	buffer_load_dwordx4 v1, s[4:7], s29 offen lds
	s_mov_b32 m0, s42
	s_nop 0
	buffer_load_dwordx4 v175, s[4:7], s29 offen lds
	s_waitcnt vmcnt(8)
	s_waitcnt lgkmcnt(0)
	s_barrier
	v_mfma_f32_16x16x32_bf16 v[62:65], v[162:165], v[210:213], v[62:65]
	v_mfma_f32_16x16x32_bf16 v[58:61], v[186:189], v[210:213], v[58:61]
	v_mfma_f32_16x16x32_bf16 v[50:53], v[186:189], v[218:221], v[50:53]
	v_mfma_f32_16x16x32_bf16 v[54:57], v[162:165], v[218:221], v[54:57]
	v_mfma_f32_16x16x32_bf16 v[46:49], v[162:165], v[226:229], v[46:49]
	v_mfma_f32_16x16x32_bf16 v[42:45], v[186:189], v[226:229], v[42:45]
	v_mfma_f32_16x16x32_bf16 v[34:37], v[186:189], v[234:237], v[34:37]
	v_mfma_f32_16x16x32_bf16 v[38:41], v[162:165], v[234:237], v[38:41]
	v_mfma_f32_16x16x32_bf16 v[62:65], v[182:185], v[214:217], v[62:65]
	v_mfma_f32_16x16x32_bf16 v[58:61], v[190:193], v[214:217], v[58:61]
	v_mfma_f32_16x16x32_bf16 v[50:53], v[190:193], v[222:225], v[50:53]
	v_mfma_f32_16x16x32_bf16 v[54:57], v[182:185], v[222:225], v[54:57]
	v_mfma_f32_16x16x32_bf16 v[46:49], v[182:185], v[230:233], v[46:49]
	v_mfma_f32_16x16x32_bf16 v[42:45], v[190:193], v[230:233], v[42:45]
	v_mfma_f32_16x16x32_bf16 v[34:37], v[190:193], v[238:241], v[34:37]
	v_mfma_f32_16x16x32_bf16 v[38:41], v[182:185], v[238:241], v[38:41]
	v_mfma_f32_16x16x32_bf16 v[30:33], v[194:197], v[210:213], v[30:33]
	v_mfma_f32_16x16x32_bf16 v[26:29], v[202:205], v[210:213], v[26:29]
	v_mfma_f32_16x16x32_bf16 v[18:21], v[202:205], v[218:221], v[18:21]
	v_mfma_f32_16x16x32_bf16 v[22:25], v[194:197], v[218:221], v[22:25]
	v_mfma_f32_16x16x32_bf16 v[14:17], v[194:197], v[226:229], v[14:17]
	v_mfma_f32_16x16x32_bf16 v[10:13], v[202:205], v[226:229], v[10:13]
	v_mfma_f32_16x16x32_bf16 v[2:5], v[202:205], v[234:237], v[2:5]
	v_mfma_f32_16x16x32_bf16 v[6:9], v[194:197], v[234:237], v[6:9]
	v_mfma_f32_16x16x32_bf16 v[30:33], v[198:201], v[214:217], v[30:33]
	v_mfma_f32_16x16x32_bf16 v[26:29], v[206:209], v[214:217], v[26:29]
	v_mfma_f32_16x16x32_bf16 v[18:21], v[206:209], v[222:225], v[18:21]
	v_mfma_f32_16x16x32_bf16 v[22:25], v[198:201], v[222:225], v[22:25]
	v_mfma_f32_16x16x32_bf16 v[14:17], v[198:201], v[230:233], v[14:17]
	v_mfma_f32_16x16x32_bf16 v[10:13], v[206:209], v[230:233], v[10:13]
	v_mfma_f32_16x16x32_bf16 v[2:5], v[206:209], v[238:241], v[2:5]
	v_mfma_f32_16x16x32_bf16 v[6:9], v[198:201], v[238:241], v[6:9]
	s_barrier
	v_add_u32_e32 v166, 0x18000, v179
	ds_read_b128 v[162:165], v166
	ds_read_b128 v[182:185], v166 offset:1024
	ds_read_b128 v[186:189], v166 offset:2048
	ds_read_b128 v[190:193], v166 offset:3072
	v_add_u32_e32 v166, 0x1c000, v179
	ds_read_b128 v[194:197], v166
	ds_read_b128 v[198:201], v166 offset:1024
	ds_read_b128 v[202:205], v166 offset:2048
	ds_read_b128 v[206:209], v166 offset:3072
	s_add_i32 s29, s29, 0x80000
	s_mov_b32 m0, s43
	ds_read_b128 v[210:213], v180 offset:32768
	ds_read_b128 v[214:217], v180 offset:33792
	ds_read_b128 v[218:221], v180 offset:34816
	ds_read_b128 v[222:225], v180 offset:35840
	ds_read_b128 v[226:229], v180 offset:36864
	ds_read_b128 v[230:233], v180 offset:37888
	ds_read_b128 v[234:237], v180 offset:38912
	ds_read_b128 v[238:241], v180 offset:39936
	buffer_load_dwordx4 v1, s[4:7], s29 offen lds
	s_mov_b32 m0, s44
	s_nop 0
	buffer_load_dwordx4 v175, s[4:7], s29 offen lds
	s_waitcnt vmcnt(8)
	s_waitcnt lgkmcnt(0)
	s_barrier
	v_mfma_f32_16x16x32_bf16 v[126:129], v[162:165], v[210:213], v[126:129]
	v_mfma_f32_16x16x32_bf16 v[122:125], v[186:189], v[210:213], v[122:125]
	v_mfma_f32_16x16x32_bf16 v[114:117], v[186:189], v[218:221], v[114:117]
	v_mfma_f32_16x16x32_bf16 v[118:121], v[162:165], v[218:221], v[118:121]
	v_mfma_f32_16x16x32_bf16 v[110:113], v[162:165], v[226:229], v[110:113]
	v_mfma_f32_16x16x32_bf16 v[106:109], v[186:189], v[226:229], v[106:109]
	v_mfma_f32_16x16x32_bf16 v[98:101], v[186:189], v[234:237], v[98:101]
	v_mfma_f32_16x16x32_bf16 v[102:105], v[162:165], v[234:237], v[102:105]
	v_mfma_f32_16x16x32_bf16 v[126:129], v[182:185], v[214:217], v[126:129]
	v_mfma_f32_16x16x32_bf16 v[122:125], v[190:193], v[214:217], v[122:125]
	v_mfma_f32_16x16x32_bf16 v[114:117], v[190:193], v[222:225], v[114:117]
	v_mfma_f32_16x16x32_bf16 v[118:121], v[182:185], v[222:225], v[118:121]
	v_mfma_f32_16x16x32_bf16 v[110:113], v[182:185], v[230:233], v[110:113]
	v_mfma_f32_16x16x32_bf16 v[106:109], v[190:193], v[230:233], v[106:109]
	v_mfma_f32_16x16x32_bf16 v[98:101], v[190:193], v[238:241], v[98:101]
	v_mfma_f32_16x16x32_bf16 v[102:105], v[182:185], v[238:241], v[102:105]
	v_mfma_f32_16x16x32_bf16 v[94:97], v[194:197], v[210:213], v[94:97]
	v_mfma_f32_16x16x32_bf16 v[90:93], v[202:205], v[210:213], v[90:93]
	v_mfma_f32_16x16x32_bf16 v[82:85], v[202:205], v[218:221], v[82:85]
	v_mfma_f32_16x16x32_bf16 v[86:89], v[194:197], v[218:221], v[86:89]
	v_mfma_f32_16x16x32_bf16 v[78:81], v[194:197], v[226:229], v[78:81]
	v_mfma_f32_16x16x32_bf16 v[74:77], v[202:205], v[226:229], v[74:77]
	v_mfma_f32_16x16x32_bf16 v[66:69], v[202:205], v[234:237], v[66:69]
	v_mfma_f32_16x16x32_bf16 v[70:73], v[194:197], v[234:237], v[70:73]
	v_mfma_f32_16x16x32_bf16 v[94:97], v[198:201], v[214:217], v[94:97]
	v_mfma_f32_16x16x32_bf16 v[90:93], v[206:209], v[214:217], v[90:93]
	v_mfma_f32_16x16x32_bf16 v[82:85], v[206:209], v[222:225], v[82:85]
	v_mfma_f32_16x16x32_bf16 v[86:89], v[198:201], v[222:225], v[86:89]
	v_mfma_f32_16x16x32_bf16 v[78:81], v[198:201], v[230:233], v[78:81]
	v_mfma_f32_16x16x32_bf16 v[74:77], v[206:209], v[230:233], v[74:77]
	v_mfma_f32_16x16x32_bf16 v[66:69], v[206:209], v[238:241], v[66:69]
	v_mfma_f32_16x16x32_bf16 v[70:73], v[198:201], v[238:241], v[70:73]
	s_barrier
	s_mov_b32 m0, s49
	ds_read_b128 v[210:213], v180 offset:49152
	ds_read_b128 v[214:217], v180 offset:50176
	ds_read_b128 v[218:221], v180 offset:51200
	ds_read_b128 v[222:225], v180 offset:52224
	ds_read_b128 v[226:229], v180 offset:53248
	ds_read_b128 v[230:233], v180 offset:54272
	ds_read_b128 v[234:237], v180 offset:55296
	ds_read_b128 v[238:241], v180 offset:56320
	buffer_load_dwordx4 v174, s[8:11], s28 offen lds
	s_mov_b32 m0, s50
	s_add_i32 s27, s27, 0x80080
	buffer_load_dwordx4 v176, s[8:11], s28 offen lds
	s_mov_b32 m0, s53
	s_nop 0
	buffer_load_dwordx4 v174, s[8:11], s27 offen lds
	s_mov_b32 m0, s54
	s_nop 0
	buffer_load_dwordx4 v176, s[8:11], s27 offen lds
	s_mov_b32 m0, s51
	s_nop 0
	buffer_load_dwordx4 v1, s[4:7], s26 offen lds
	s_mov_b32 m0, s52
	s_nop 0
	buffer_load_dwordx4 v175, s[4:7], s26 offen lds
	s_waitcnt vmcnt(8)
	s_waitcnt lgkmcnt(0)
	s_barrier
	v_mfma_f32_16x16x32_bf16 v[62:65], v[162:165], v[210:213], v[62:65]
	v_mfma_f32_16x16x32_bf16 v[58:61], v[186:189], v[210:213], v[58:61]
	v_mfma_f32_16x16x32_bf16 v[50:53], v[186:189], v[218:221], v[50:53]
	v_mfma_f32_16x16x32_bf16 v[54:57], v[162:165], v[218:221], v[54:57]
	v_mfma_f32_16x16x32_bf16 v[46:49], v[162:165], v[226:229], v[46:49]
	v_mfma_f32_16x16x32_bf16 v[42:45], v[186:189], v[226:229], v[42:45]
	v_mfma_f32_16x16x32_bf16 v[34:37], v[186:189], v[234:237], v[34:37]
	v_mfma_f32_16x16x32_bf16 v[38:41], v[162:165], v[234:237], v[38:41]
	v_mfma_f32_16x16x32_bf16 v[62:65], v[182:185], v[214:217], v[62:65]
	v_mfma_f32_16x16x32_bf16 v[58:61], v[190:193], v[214:217], v[58:61]
	v_mfma_f32_16x16x32_bf16 v[50:53], v[190:193], v[222:225], v[50:53]
	v_mfma_f32_16x16x32_bf16 v[54:57], v[182:185], v[222:225], v[54:57]
	v_mfma_f32_16x16x32_bf16 v[46:49], v[182:185], v[230:233], v[46:49]
	v_mfma_f32_16x16x32_bf16 v[42:45], v[190:193], v[230:233], v[42:45]
	v_mfma_f32_16x16x32_bf16 v[34:37], v[190:193], v[238:241], v[34:37]
	v_mfma_f32_16x16x32_bf16 v[38:41], v[182:185], v[238:241], v[38:41]
	v_mfma_f32_16x16x32_bf16 v[30:33], v[194:197], v[210:213], v[30:33]
	v_mfma_f32_16x16x32_bf16 v[26:29], v[202:205], v[210:213], v[26:29]
	v_mfma_f32_16x16x32_bf16 v[18:21], v[202:205], v[218:221], v[18:21]
	v_mfma_f32_16x16x32_bf16 v[22:25], v[194:197], v[218:221], v[22:25]
	v_mfma_f32_16x16x32_bf16 v[14:17], v[194:197], v[226:229], v[14:17]
	v_mfma_f32_16x16x32_bf16 v[10:13], v[202:205], v[226:229], v[10:13]
	v_mfma_f32_16x16x32_bf16 v[2:5], v[202:205], v[234:237], v[2:5]
	v_mfma_f32_16x16x32_bf16 v[6:9], v[194:197], v[234:237], v[6:9]
	v_mfma_f32_16x16x32_bf16 v[30:33], v[198:201], v[214:217], v[30:33]
	v_mfma_f32_16x16x32_bf16 v[26:29], v[206:209], v[214:217], v[26:29]
	v_mfma_f32_16x16x32_bf16 v[18:21], v[206:209], v[222:225], v[18:21]
	v_mfma_f32_16x16x32_bf16 v[22:25], v[198:201], v[222:225], v[22:25]
	v_mfma_f32_16x16x32_bf16 v[14:17], v[198:201], v[230:233], v[14:17]
	v_mfma_f32_16x16x32_bf16 v[10:13], v[206:209], v[230:233], v[10:13]
	v_mfma_f32_16x16x32_bf16 v[2:5], v[206:209], v[238:241], v[2:5]
	v_mfma_f32_16x16x32_bf16 v[6:9], v[198:201], v[238:241], v[6:9]
	s_barrier
	s_add_i32 s10, s65, 2
	s_addk_i32 s64, 0x100
	s_cmp_gt_u32 s65, 29
	s_cbranch_scc1 .LBB0_910
	s_mov_b32 s65, s10
	s_branch .LBB0_869

.LBB0_1029:
	v_add_u32_e32 v152, 0x10000, v138
	v_add_u32_e32 v168, 0x14000, v138
	ds_read_b128 v[140:143], v152
	ds_read_b128 v[144:147], v152 offset:1024
	ds_read_b128 v[148:151], v152 offset:2048
	ds_read_b128 v[152:155], v152 offset:3072
	ds_read_b128 v[156:159], v168
	ds_read_b128 v[160:163], v168 offset:1024
	ds_read_b128 v[164:167], v168 offset:2048
	ds_read_b128 v[168:171], v168 offset:3072
	s_add_i32 s10, s30, s50
	s_add_i32 s51, s25, s50
	s_add_i32 s11, s10, 0x4000
	s_addk_i32 s51, 0x4000
	s_cmp_eq_u32 s50, 0
	s_cselect_b32 s53, s47, s11
	s_cselect_b32 s52, s48, s51
	s_or_b32 s51, s53, 0x80
	s_add_i32 s10, s10, 0x203f80
	s_mov_b32 m0, s41
	ds_read_b128 v[172:175], v139
	ds_read_b128 v[176:179], v139 offset:1024
	ds_read_b128 v[180:183], v139 offset:2048
	ds_read_b128 v[184:187], v139 offset:3072
	ds_read_b128 v[188:191], v139 offset:4096
	ds_read_b128 v[192:195], v139 offset:5120
	ds_read_b128 v[196:199], v139 offset:6144
	ds_read_b128 v[200:203], v139 offset:7168
	buffer_load_dwordx4 v134, s[4:7], s10 offen lds
	s_mov_b32 m0, s42
	s_nop 0
	buffer_load_dwordx4 v136, s[4:7], s10 offen lds
	s_waitcnt vmcnt(8)
	s_waitcnt lgkmcnt(0)
	s_barrier
	v_mfma_f32_16x16x32_bf16 v[126:129], v[140:143], v[172:175], v[126:129]
	v_mfma_f32_16x16x32_bf16 v[122:125], v[148:151], v[172:175], v[122:125]
	v_mfma_f32_16x16x32_bf16 v[106:109], v[148:151], v[180:183], v[106:109]
	v_mfma_f32_16x16x32_bf16 v[114:117], v[140:143], v[180:183], v[114:117]
	v_mfma_f32_16x16x32_bf16 v[98:101], v[140:143], v[188:191], v[98:101]
	v_mfma_f32_16x16x32_bf16 v[90:93], v[148:151], v[188:191], v[90:93]
	v_mfma_f32_16x16x32_bf16 v[74:77], v[148:151], v[196:199], v[74:77]
	v_mfma_f32_16x16x32_bf16 v[82:85], v[140:143], v[196:199], v[82:85]
	v_mfma_f32_16x16x32_bf16 v[126:129], v[144:147], v[176:179], v[126:129]
	v_mfma_f32_16x16x32_bf16 v[122:125], v[152:155], v[176:179], v[122:125]
	v_mfma_f32_16x16x32_bf16 v[106:109], v[152:155], v[184:187], v[106:109]
	v_mfma_f32_16x16x32_bf16 v[114:117], v[144:147], v[184:187], v[114:117]
	v_mfma_f32_16x16x32_bf16 v[98:101], v[144:147], v[192:195], v[98:101]
	v_mfma_f32_16x16x32_bf16 v[90:93], v[152:155], v[192:195], v[90:93]
	v_mfma_f32_16x16x32_bf16 v[74:77], v[152:155], v[200:203], v[74:77]
	v_mfma_f32_16x16x32_bf16 v[82:85], v[144:147], v[200:203], v[82:85]
	v_mfma_f32_16x16x32_bf16 v[118:121], v[156:159], v[172:175], v[118:121]
	v_mfma_f32_16x16x32_bf16 v[110:113], v[164:167], v[172:175], v[110:113]
	v_mfma_f32_16x16x32_bf16 v[94:97], v[164:167], v[180:183], v[94:97]
	v_mfma_f32_16x16x32_bf16 v[102:105], v[156:159], v[180:183], v[102:105]
	v_mfma_f32_16x16x32_bf16 v[86:89], v[156:159], v[188:191], v[86:89]
	v_mfma_f32_16x16x32_bf16 v[78:81], v[164:167], v[188:191], v[78:81]
	v_mfma_f32_16x16x32_bf16 v[66:69], v[164:167], v[196:199], v[66:69]
	v_mfma_f32_16x16x32_bf16 v[70:73], v[156:159], v[196:199], v[70:73]
	v_mfma_f32_16x16x32_bf16 v[118:121], v[160:163], v[176:179], v[118:121]
	v_mfma_f32_16x16x32_bf16 v[110:113], v[168:171], v[176:179], v[110:113]
	v_mfma_f32_16x16x32_bf16 v[94:97], v[168:171], v[184:187], v[94:97]
	v_mfma_f32_16x16x32_bf16 v[102:105], v[160:163], v[184:187], v[102:105]
	v_mfma_f32_16x16x32_bf16 v[86:89], v[160:163], v[192:195], v[86:89]
	v_mfma_f32_16x16x32_bf16 v[78:81], v[168:171], v[192:195], v[78:81]
	v_mfma_f32_16x16x32_bf16 v[66:69], v[168:171], v[200:203], v[66:69]
	v_mfma_f32_16x16x32_bf16 v[70:73], v[160:163], v[200:203], v[70:73]
	s_barrier
	s_mov_b32 m0, s24
	s_mov_b32 s10, s6
	s_mov_b32 s11, s7
	ds_read_b128 v[172:175], v139 offset:16384
	ds_read_b128 v[176:179], v139 offset:17408
	ds_read_b128 v[180:183], v139 offset:18432
	ds_read_b128 v[184:187], v139 offset:19456
	ds_read_b128 v[188:191], v139 offset:20480
	ds_read_b128 v[192:195], v139 offset:21504
	ds_read_b128 v[196:199], v139 offset:22528
	ds_read_b128 v[200:203], v139 offset:23552
	buffer_load_dwordx4 v135, s[8:11], s52 offen lds
	s_mov_b32 m0, s26
	s_add_i32 s54, s52, 0x200000
	buffer_load_dwordx4 v137, s[8:11], s52 offen lds
	s_mov_b32 m0, s27
	s_nop 0
	buffer_load_dwordx4 v135, s[8:11], s54 offen lds
	s_mov_b32 m0, s28
	s_nop 0
	buffer_load_dwordx4 v137, s[8:11], s54 offen lds
	s_mov_b32 m0, s23
	s_nop 0
	buffer_load_dwordx4 v134, s[4:7], s53 offen lds
	s_mov_b32 m0, s29
	s_nop 0
	buffer_load_dwordx4 v136, s[4:7], s53 offen lds
	s_waitcnt vmcnt(8)
	s_waitcnt lgkmcnt(0)
	s_barrier
	v_mfma_f32_16x16x32_bf16 v[62:65], v[140:143], v[172:175], v[62:65]
	v_mfma_f32_16x16x32_bf16 v[58:61], v[148:151], v[172:175], v[58:61]
	v_mfma_f32_16x16x32_bf16 v[42:45], v[148:151], v[180:183], v[42:45]
	v_mfma_f32_16x16x32_bf16 v[50:53], v[140:143], v[180:183], v[50:53]
	v_mfma_f32_16x16x32_bf16 v[34:37], v[140:143], v[188:191], v[34:37]
	v_mfma_f32_16x16x32_bf16 v[26:29], v[148:151], v[188:191], v[26:29]
	v_mfma_f32_16x16x32_bf16 v[10:13], v[148:151], v[196:199], v[10:13]
	v_mfma_f32_16x16x32_bf16 v[18:21], v[140:143], v[196:199], v[18:21]
	v_mfma_f32_16x16x32_bf16 v[62:65], v[144:147], v[176:179], v[62:65]
	v_mfma_f32_16x16x32_bf16 v[58:61], v[152:155], v[176:179], v[58:61]
	v_mfma_f32_16x16x32_bf16 v[42:45], v[152:155], v[184:187], v[42:45]
	v_mfma_f32_16x16x32_bf16 v[50:53], v[144:147], v[184:187], v[50:53]
	v_mfma_f32_16x16x32_bf16 v[34:37], v[144:147], v[192:195], v[34:37]
	v_mfma_f32_16x16x32_bf16 v[26:29], v[152:155], v[192:195], v[26:29]
	v_mfma_f32_16x16x32_bf16 v[10:13], v[152:155], v[200:203], v[10:13]
	v_mfma_f32_16x16x32_bf16 v[18:21], v[144:147], v[200:203], v[18:21]
	v_mfma_f32_16x16x32_bf16 v[54:57], v[156:159], v[172:175], v[54:57]
	v_mfma_f32_16x16x32_bf16 v[46:49], v[164:167], v[172:175], v[46:49]
	v_mfma_f32_16x16x32_bf16 v[30:33], v[164:167], v[180:183], v[30:33]
	v_mfma_f32_16x16x32_bf16 v[38:41], v[156:159], v[180:183], v[38:41]
	v_mfma_f32_16x16x32_bf16 v[22:25], v[156:159], v[188:191], v[22:25]
	v_mfma_f32_16x16x32_bf16 v[14:17], v[164:167], v[188:191], v[14:17]
	v_mfma_f32_16x16x32_bf16 v[2:5], v[164:167], v[196:199], v[2:5]
	v_mfma_f32_16x16x32_bf16 v[6:9], v[156:159], v[196:199], v[6:9]
	v_mfma_f32_16x16x32_bf16 v[54:57], v[160:163], v[176:179], v[54:57]
	v_mfma_f32_16x16x32_bf16 v[46:49], v[168:171], v[176:179], v[46:49]
	v_mfma_f32_16x16x32_bf16 v[30:33], v[168:171], v[184:187], v[30:33]
	v_mfma_f32_16x16x32_bf16 v[38:41], v[160:163], v[184:187], v[38:41]
	v_mfma_f32_16x16x32_bf16 v[22:25], v[160:163], v[192:195], v[22:25]
	v_mfma_f32_16x16x32_bf16 v[14:17], v[168:171], v[192:195], v[14:17]
	v_mfma_f32_16x16x32_bf16 v[2:5], v[168:171], v[200:203], v[2:5]
	v_mfma_f32_16x16x32_bf16 v[6:9], v[160:163], v[200:203], v[6:9]
	s_barrier
	v_add_u32_e32 v152, 0x18000, v138
	v_add_u32_e32 v168, 0x1c000, v138
	ds_read_b128 v[140:143], v152
	ds_read_b128 v[144:147], v152 offset:1024
	ds_read_b128 v[148:151], v152 offset:2048
	ds_read_b128 v[152:155], v152 offset:3072
	ds_read_b128 v[156:159], v168
	ds_read_b128 v[160:163], v168 offset:1024
	ds_read_b128 v[164:167], v168 offset:2048
	ds_read_b128 v[168:171], v168 offset:3072
	s_add_i32 s53, s53, 0x200000
	s_mov_b32 m0, s31
	ds_read_b128 v[172:175], v139 offset:32768
	ds_read_b128 v[176:179], v139 offset:33792
	ds_read_b128 v[180:183], v139 offset:34816
	ds_read_b128 v[184:187], v139 offset:35840
	ds_read_b128 v[188:191], v139 offset:36864
	ds_read_b128 v[192:195], v139 offset:37888
	ds_read_b128 v[196:199], v139 offset:38912
	ds_read_b128 v[200:203], v139 offset:39936
	buffer_load_dwordx4 v134, s[4:7], s53 offen lds
	s_mov_b32 m0, s33
	s_nop 0
	buffer_load_dwordx4 v136, s[4:7], s53 offen lds
	s_waitcnt vmcnt(8)
	s_waitcnt lgkmcnt(0)
	s_barrier
	v_mfma_f32_16x16x32_bf16 v[126:129], v[140:143], v[172:175], v[126:129]
	v_mfma_f32_16x16x32_bf16 v[122:125], v[148:151], v[172:175], v[122:125]
	v_mfma_f32_16x16x32_bf16 v[106:109], v[148:151], v[180:183], v[106:109]
	v_mfma_f32_16x16x32_bf16 v[114:117], v[140:143], v[180:183], v[114:117]
	v_mfma_f32_16x16x32_bf16 v[98:101], v[140:143], v[188:191], v[98:101]
	v_mfma_f32_16x16x32_bf16 v[90:93], v[148:151], v[188:191], v[90:93]
	v_mfma_f32_16x16x32_bf16 v[74:77], v[148:151], v[196:199], v[74:77]
	v_mfma_f32_16x16x32_bf16 v[82:85], v[140:143], v[196:199], v[82:85]
	v_mfma_f32_16x16x32_bf16 v[126:129], v[144:147], v[176:179], v[126:129]
	v_mfma_f32_16x16x32_bf16 v[122:125], v[152:155], v[176:179], v[122:125]
	v_mfma_f32_16x16x32_bf16 v[106:109], v[152:155], v[184:187], v[106:109]
	v_mfma_f32_16x16x32_bf16 v[114:117], v[144:147], v[184:187], v[114:117]
	v_mfma_f32_16x16x32_bf16 v[98:101], v[144:147], v[192:195], v[98:101]
	v_mfma_f32_16x16x32_bf16 v[90:93], v[152:155], v[192:195], v[90:93]
	v_mfma_f32_16x16x32_bf16 v[74:77], v[152:155], v[200:203], v[74:77]
	v_mfma_f32_16x16x32_bf16 v[82:85], v[144:147], v[200:203], v[82:85]
	v_mfma_f32_16x16x32_bf16 v[118:121], v[156:159], v[172:175], v[118:121]
	v_mfma_f32_16x16x32_bf16 v[110:113], v[164:167], v[172:175], v[110:113]
	v_mfma_f32_16x16x32_bf16 v[94:97], v[164:167], v[180:183], v[94:97]
	v_mfma_f32_16x16x32_bf16 v[102:105], v[156:159], v[180:183], v[102:105]
	v_mfma_f32_16x16x32_bf16 v[86:89], v[156:159], v[188:191], v[86:89]
	v_mfma_f32_16x16x32_bf16 v[78:81], v[164:167], v[188:191], v[78:81]
	v_mfma_f32_16x16x32_bf16 v[66:69], v[164:167], v[196:199], v[66:69]
	v_mfma_f32_16x16x32_bf16 v[70:73], v[156:159], v[196:199], v[70:73]
	v_mfma_f32_16x16x32_bf16 v[118:121], v[160:163], v[176:179], v[118:121]
	v_mfma_f32_16x16x32_bf16 v[110:113], v[168:171], v[176:179], v[110:113]
	v_mfma_f32_16x16x32_bf16 v[94:97], v[168:171], v[184:187], v[94:97]
	v_mfma_f32_16x16x32_bf16 v[102:105], v[160:163], v[184:187], v[102:105]
	v_mfma_f32_16x16x32_bf16 v[86:89], v[160:163], v[192:195], v[86:89]
	v_mfma_f32_16x16x32_bf16 v[78:81], v[168:171], v[192:195], v[78:81]
	v_mfma_f32_16x16x32_bf16 v[66:69], v[168:171], v[200:203], v[66:69]
	v_mfma_f32_16x16x32_bf16 v[70:73], v[160:163], v[200:203], v[70:73]
	s_barrier
	s_mov_b32 m0, s34
	s_or_b32 s53, s52, 0x80
	ds_read_b128 v[172:175], v139 offset:49152
	ds_read_b128 v[176:179], v139 offset:50176
	ds_read_b128 v[180:183], v139 offset:51200
	ds_read_b128 v[184:187], v139 offset:52224
	ds_read_b128 v[188:191], v139 offset:53248
	ds_read_b128 v[192:195], v139 offset:54272
	ds_read_b128 v[196:199], v139 offset:55296
	ds_read_b128 v[200:203], v139 offset:56320
	buffer_load_dwordx4 v135, s[8:11], s53 offen lds
	s_mov_b32 m0, s35
	s_add_i32 s52, s52, 0x200080
	buffer_load_dwordx4 v137, s[8:11], s53 offen lds
	s_mov_b32 m0, s39
	s_nop 0
	buffer_load_dwordx4 v135, s[8:11], s52 offen lds
	s_mov_b32 m0, s40
	s_nop 0
	buffer_load_dwordx4 v137, s[8:11], s52 offen lds
	s_mov_b32 m0, s37
	s_nop 0
	buffer_load_dwordx4 v134, s[4:7], s51 offen lds
	s_mov_b32 m0, s38
	s_nop 0
	buffer_load_dwordx4 v136, s[4:7], s51 offen lds
	s_waitcnt vmcnt(8)
	s_waitcnt lgkmcnt(0)
	s_barrier
	v_mfma_f32_16x16x32_bf16 v[62:65], v[140:143], v[172:175], v[62:65]
	v_mfma_f32_16x16x32_bf16 v[58:61], v[148:151], v[172:175], v[58:61]
	v_mfma_f32_16x16x32_bf16 v[42:45], v[148:151], v[180:183], v[42:45]
	v_mfma_f32_16x16x32_bf16 v[50:53], v[140:143], v[180:183], v[50:53]
	v_mfma_f32_16x16x32_bf16 v[34:37], v[140:143], v[188:191], v[34:37]
	v_mfma_f32_16x16x32_bf16 v[26:29], v[148:151], v[188:191], v[26:29]
	v_mfma_f32_16x16x32_bf16 v[10:13], v[148:151], v[196:199], v[10:13]
	v_mfma_f32_16x16x32_bf16 v[18:21], v[140:143], v[196:199], v[18:21]
	v_mfma_f32_16x16x32_bf16 v[62:65], v[144:147], v[176:179], v[62:65]
	v_mfma_f32_16x16x32_bf16 v[58:61], v[152:155], v[176:179], v[58:61]
	v_mfma_f32_16x16x32_bf16 v[42:45], v[152:155], v[184:187], v[42:45]
	v_mfma_f32_16x16x32_bf16 v[50:53], v[144:147], v[184:187], v[50:53]
	v_mfma_f32_16x16x32_bf16 v[34:37], v[144:147], v[192:195], v[34:37]
	v_mfma_f32_16x16x32_bf16 v[26:29], v[152:155], v[192:195], v[26:29]
	v_mfma_f32_16x16x32_bf16 v[10:13], v[152:155], v[200:203], v[10:13]
	v_mfma_f32_16x16x32_bf16 v[18:21], v[144:147], v[200:203], v[18:21]
	v_mfma_f32_16x16x32_bf16 v[54:57], v[156:159], v[172:175], v[54:57]
	v_mfma_f32_16x16x32_bf16 v[46:49], v[164:167], v[172:175], v[46:49]
	v_mfma_f32_16x16x32_bf16 v[30:33], v[164:167], v[180:183], v[30:33]
	v_mfma_f32_16x16x32_bf16 v[38:41], v[156:159], v[180:183], v[38:41]
	v_mfma_f32_16x16x32_bf16 v[22:25], v[156:159], v[188:191], v[22:25]
	v_mfma_f32_16x16x32_bf16 v[14:17], v[164:167], v[188:191], v[14:17]
	v_mfma_f32_16x16x32_bf16 v[2:5], v[164:167], v[196:199], v[2:5]
	v_mfma_f32_16x16x32_bf16 v[6:9], v[156:159], v[196:199], v[6:9]
	v_mfma_f32_16x16x32_bf16 v[54:57], v[160:163], v[176:179], v[54:57]
	v_mfma_f32_16x16x32_bf16 v[46:49], v[168:171], v[176:179], v[46:49]
	v_mfma_f32_16x16x32_bf16 v[30:33], v[168:171], v[184:187], v[30:33]
	v_mfma_f32_16x16x32_bf16 v[38:41], v[160:163], v[184:187], v[38:41]
	v_mfma_f32_16x16x32_bf16 v[22:25], v[160:163], v[192:195], v[22:25]
	v_mfma_f32_16x16x32_bf16 v[14:17], v[168:171], v[192:195], v[14:17]
	v_mfma_f32_16x16x32_bf16 v[2:5], v[168:171], v[200:203], v[2:5]
	v_mfma_f32_16x16x32_bf16 v[6:9], v[160:163], v[200:203], v[6:9]
	s_barrier
	s_add_i32 s49, s49, 2
	s_addk_i32 s50, 0x100
	s_cmpk_gt_u32 s49, 0x7d
	s_cbranch_scc0 .LBB0_1029
	s_andn2_b64 vcc, exec, s[2:3]
	s_cbranch_vccnz .LBB0_1021
	v_mov_b32_e32 v2, 0
	s_mov_b32 s17, s44
	s_mov_b32 s14, s45
	s_mov_b32 s25, s46
	s_mov_b32 s30, s13
	s_mov_b32 s43, s12
	v_mov_b32_e32 v3, v2
	v_mov_b32_e32 v4, v2
	v_mov_b32_e32 v5, v2
	v_mov_b32_e32 v6, v2
	v_mov_b32_e32 v7, v2
	v_mov_b32_e32 v8, v2
	v_mov_b32_e32 v9, v2
	v_mov_b32_e32 v14, v2
	v_mov_b32_e32 v15, v2
	v_mov_b32_e32 v16, v2
	v_mov_b32_e32 v17, v2
	v_mov_b32_e32 v22, v2
	v_mov_b32_e32 v23, v2
	v_mov_b32_e32 v24, v2
	v_mov_b32_e32 v25, v2
	v_mov_b32_e32 v30, v2
	v_mov_b32_e32 v31, v2
	v_mov_b32_e32 v32, v2
	v_mov_b32_e32 v33, v2
	v_mov_b32_e32 v38, v2
	v_mov_b32_e32 v39, v2
	v_mov_b32_e32 v40, v2
	v_mov_b32_e32 v41, v2
	v_mov_b32_e32 v46, v2
	v_mov_b32_e32 v47, v2
	v_mov_b32_e32 v48, v2
	v_mov_b32_e32 v49, v2
	v_mov_b32_e32 v54, v2
	v_mov_b32_e32 v55, v2
	v_mov_b32_e32 v56, v2
	v_mov_b32_e32 v57, v2
	v_mov_b32_e32 v10, v2
	v_mov_b32_e32 v11, v2
	v_mov_b32_e32 v12, v2
	v_mov_b32_e32 v13, v2
	v_mov_b32_e32 v18, v2
	v_mov_b32_e32 v19, v2
	v_mov_b32_e32 v20, v2
	v_mov_b32_e32 v21, v2
	v_mov_b32_e32 v26, v2
	v_mov_b32_e32 v27, v2
	v_mov_b32_e32 v28, v2
	v_mov_b32_e32 v29, v2
	v_mov_b32_e32 v34, v2
	v_mov_b32_e32 v35, v2
	v_mov_b32_e32 v36, v2
	v_mov_b32_e32 v37, v2
	v_mov_b32_e32 v42, v2
	v_mov_b32_e32 v43, v2
	v_mov_b32_e32 v44, v2
	v_mov_b32_e32 v45, v2
	v_mov_b32_e32 v50, v2
	v_mov_b32_e32 v51, v2
	v_mov_b32_e32 v52, v2
	v_mov_b32_e32 v53, v2
	v_mov_b32_e32 v58, v2
	v_mov_b32_e32 v59, v2
	v_mov_b32_e32 v60, v2
	v_mov_b32_e32 v61, v2
	v_mov_b32_e32 v62, v2
	v_mov_b32_e32 v63, v2
	v_mov_b32_e32 v64, v2
	v_mov_b32_e32 v65, v2
	v_mov_b32_e32 v66, v2
	v_mov_b32_e32 v67, v2
	v_mov_b32_e32 v68, v2
	v_mov_b32_e32 v69, v2
	v_mov_b32_e32 v70, v2
	v_mov_b32_e32 v71, v2
	v_mov_b32_e32 v72, v2
	v_mov_b32_e32 v73, v2
	v_mov_b32_e32 v78, v2
	v_mov_b32_e32 v79, v2
	v_mov_b32_e32 v80, v2
	v_mov_b32_e32 v81, v2
	v_mov_b32_e32 v86, v2
	v_mov_b32_e32 v87, v2
	v_mov_b32_e32 v88, v2
	v_mov_b32_e32 v89, v2
	v_mov_b32_e32 v94, v2
	v_mov_b32_e32 v95, v2
	v_mov_b32_e32 v96, v2
	v_mov_b32_e32 v97, v2
	v_mov_b32_e32 v102, v2
	v_mov_b32_e32 v103, v2
	v_mov_b32_e32 v104, v2
	v_mov_b32_e32 v105, v2
	v_mov_b32_e32 v110, v2
	v_mov_b32_e32 v111, v2
	v_mov_b32_e32 v112, v2
	v_mov_b32_e32 v113, v2
	v_mov_b32_e32 v118, v2
	v_mov_b32_e32 v119, v2
	v_mov_b32_e32 v120, v2
	v_mov_b32_e32 v121, v2
	v_mov_b32_e32 v74, v2
	v_mov_b32_e32 v75, v2
	v_mov_b32_e32 v76, v2
	v_mov_b32_e32 v77, v2
	v_mov_b32_e32 v82, v2
	v_mov_b32_e32 v83, v2
	v_mov_b32_e32 v84, v2
	v_mov_b32_e32 v85, v2
	v_mov_b32_e32 v90, v2
	v_mov_b32_e32 v91, v2
	v_mov_b32_e32 v92, v2
	v_mov_b32_e32 v93, v2
	v_mov_b32_e32 v98, v2
	v_mov_b32_e32 v99, v2
	v_mov_b32_e32 v100, v2
	v_mov_b32_e32 v101, v2
	v_mov_b32_e32 v106, v2
	v_mov_b32_e32 v107, v2
	v_mov_b32_e32 v108, v2
	v_mov_b32_e32 v109, v2
	v_mov_b32_e32 v114, v2
	v_mov_b32_e32 v115, v2
	v_mov_b32_e32 v116, v2
	v_mov_b32_e32 v117, v2
	v_mov_b32_e32 v122, v2
	v_mov_b32_e32 v123, v2
	v_mov_b32_e32 v124, v2
	v_mov_b32_e32 v125, v2
	v_mov_b32_e32 v126, v2
	v_mov_b32_e32 v127, v2
	v_mov_b32_e32 v128, v2
	v_mov_b32_e32 v129, v2
	s_branch .LBB0_1021
